# mLSTM-out: 30 more interleaved exact 1.0/x sigmoid divisions replaced by v_rcp_f32 (dataflow-traced), deleted ops left as s_nop
# baseline (speedup 1.0000x reference)
; #define LAS __attribute__((address_space(3)))
; __device__ __forceinline__ unsigned pk2(float lo, float hi) { return __builtin_amdgcn_perm(__builtin_bit_cast(unsigned, hi) + 0x8000u, __builtin_bit_cast(unsigned, lo) + 0x8000u, 0x07060302u); }
; __device__ __forceinline__ float sigmoidf_(float x) { return 1.0f / (1.0f + __expf(-x)); }
; __device__ __forceinline__ void ph_mlstm_out(const Frame& F) {
;     ...
;         for (int tt = 0; tt < 8; ++tt) {
;             const int t = 16 * tt + l15;
;             const v2u ogc[2] = {ogn0, ogn1};
;             if (tt < 7) { ogn0 = *(const v2u*)(ogp + (size_t)(16 * (tt + 1)) * 6144); ogn1 = *(const v2u*)(ogp + (size_t)(16 * (tt + 1)) * 6144 + 16); }
;             bf16x8 qf[4];
; #pragma unroll
;             for (int st = 0; st < 4; ++st) qf[st] = *(const LAS bf16x8*)(lds + MLO_Q_OFF + t * ML_ROW + 16 * g + 64 * st);
;             const int nst = (tt >> 1) + 1;
;             bf16x8 pf[4];
; #pragma unroll
;             for (int st = 0; st < 4; ++st) if (st < nst) pf[st] = *(const LAS bf16x8*)(lds + ML_K_OFF + t * ML_ROW + 16 * g + 64 * st);
;             const float ai = ais[t], rd = rds[t];
; #pragma unroll
;             for (int vt = 0; vt < 2; ++vt) {
;                 f32x4 ci = (f32x4){0.f, 0.f, 0.f, 0.f}, cx = (f32x4){0.f, 0.f, 0.f, 0.f};
; #pragma unroll
;                 for (int st = 0; st < 4; ++st) ci = __builtin_amdgcn_mfma_f32_16x16x32_bf16(cf[vt][st], qf[st], ci, 0, 0, 0);
;                 const LAS unsigned char* vr = lds + ML_V_OFF + (16 * (2 * wave + vt) + l15) * ML_ROW + 16 * g;
; #pragma unroll
;                 for (int st = 0; st < 4; ++st) if (st < nst) cx = __builtin_amdgcn_mfma_f32_16x16x32_bf16(*(const LAS bf16x8*)(vr + 64 * st), pf[st], cx, 0, 0, 0);
;                 const int vcol = h * 256 + 16 * (2 * wave + vt) + 4 * g;
;                 const v2u ogw = ogc[vt];
;                 const float y0 = (ai * ci[0] + cx[0]) * rd * sigmoidf_(bflo(ogw.x)), y1 = (ai * ci[1] + cx[1]) * rd * sigmoidf_(bfhi(ogw.x));
;                 const float y2 = (ai * ci[2] + cx[2]) * rd * sigmoidf_(bflo(ogw.y)), y3 = (ai * ci[3] + cx[3]) * rd * sigmoidf_(bfhi(ogw.y));
;                 v2u w; w.x = pk2(y0, y1); w.y = pk2(y2, y3);
;                 *(v2u*)(YB + (size_t)(t0 + t) * 2048 + vcol) = w;
;             }
;         }
.LBB0_591:
	s_lshr_b32 s62, s57, 26
	s_add_i32 s62, s56, s62
	s_ashr_i32 s62, s62, 6
	s_lshr_b32 s57, s57, 23
	s_add_i32 s56, s56, s57
	s_lshr_b32 s57, s62, 29
	s_add_i32 s57, s62, s57
	s_and_b32 s57, s57, 0xfffff8
	s_lshl_b32 s56, s56, 4
	s_sub_i32 s63, s62, s57
	s_and_b32 s56, s56, 0xffffe000
	s_lshl_b32 s57, s62, 13
	s_sub_i32 s56, s56, s57
	s_add_i32 s56, s56, s43
	v_add_u32_e32 v188, s56, v235
	v_mov_b64_e32 v[98:99], s[24:25]
	s_movk_i32 s56, 0x3000
	v_mad_i64_i32 v[98:99], s[56:57], v188, s56, v[98:99]
	s_lshl_b32 s56, s63, 8
	s_ashr_i32 s57, s56, 31
	v_lshl_add_u64 v[98:99], s[56:57], 1, v[98:99]
	v_lshl_add_u64 v[98:99], s[92:93], 1, v[98:99]
	v_lshlrev_b32_e32 v0, 1, v178
	v_lshl_add_u64 v[138:139], v[98:99], 0, v[0:1]
	s_movk_i32 s57, 0x2000
	v_add_co_u32_e32 v100, vcc, s57, v138
	s_mov_b64 s[62:63], 0x2000
	s_nop 0
	v_addc_co_u32_e32 v101, vcc, 0, v139, vcc
	v_lshl_add_u64 v[98:99], v[138:139], 0, s[62:63]
	global_load_dwordx2 v[140:141], v[100:101], off
	global_load_dwordx2 v[142:143], v[98:99], off offset:32
	v_or_b32_e32 v0, s56, v178
	s_mov_b32 s56, 0x32000
	v_add_co_u32_e32 v98, vcc, s56, v138
	v_ashrrev_i32_e32 v189, 31, v188
	s_nop 0
	v_addc_co_u32_e32 v99, vcc, 0, v139, vcc
	global_load_dwordx2 v[112:113], v[98:99], off
	global_load_dwordx2 v[106:107], v[98:99], off offset:32
	v_add_u32_e32 v98, v204, v221
	ds_read_b128 v[118:121], v98
	ds_read_b128 v[122:125], v98 offset:64
	ds_read_b128 v[126:129], v98 offset:128
	ds_read_b128 v[130:133], v98 offset:192
	ds_read_b128 v[114:117], v116 offset:4096
	s_waitcnt lgkmcnt(4)
	v_mfma_f32_16x16x32_bf16 v[134:137], v[94:97], v[118:121], 0
	ds_read_b128 v[102:105], v247 offset:38912
	v_add_u32_e32 v158, 0x800, v233
	ds_read2_b32 v[108:109], v158 offset0:128 offset1:144
	s_waitcnt lgkmcnt(5)
	v_mfma_f32_16x16x32_bf16 v[134:137], v[82:85], v[122:125], v[134:137]
	v_lshlrev_b64 v[98:99], 12, v[188:189]
	v_lshl_add_u64 v[144:145], s[22:23], 0, v[98:99]
	v_add_u32_e32 v159, 0xc00, v233
	s_waitcnt lgkmcnt(4)
	v_mfma_f32_16x16x32_bf16 v[134:137], v[86:89], v[126:129], v[134:137]
	ds_read2_b32 v[110:111], v159 offset1:16
	v_add_u32_e32 v146, s92, v0
	v_add_u32_e32 v181, v204, v234
	s_waitcnt lgkmcnt(2)
	v_mfma_f32_16x16x32_bf16 v[98:101], v[102:105], v[114:117], 0
	s_add_i32 s43, s43, s20
	v_mfma_f32_16x16x32_bf16 v[134:137], v[90:93], v[130:133], v[134:137]
	v_mfma_f32_16x16x32_bf16 v[118:121], v[78:81], v[118:121], 0
	v_mfma_f32_16x16x32_bf16 v[118:121], v[66:69], v[122:125], v[118:121]
	s_waitcnt lgkmcnt(1)
	s_nop 4
	v_fma_f32 v98, v108, v134, v98
	s_waitcnt lgkmcnt(0)
	v_mul_f32_e32 v98, v110, v98
	v_fma_f32 v99, v108, v135, v99
	v_mul_f32_e32 v99, v110, v99
	v_fma_f32 v100, v108, v136, v100
	v_mul_f32_e32 v100, v110, v100
	v_fmac_f32_e32 v101, v108, v137
	v_mul_f32_e32 v101, v110, v101
	v_mfma_f32_16x16x32_bf16 v[118:121], v[70:73], v[126:129], v[118:121]
	v_add_u32_e32 v122, s36, v0
	s_waitcnt vmcnt(3)
	v_lshlrev_b32_e32 v134, 16, v140
	v_mul_f32_e32 v134, 0xbfb8aa3b, v134
	v_exp_f32_e32 v134, v134
	v_mfma_f32_16x16x32_bf16 v[118:121], v[74:77], v[130:133], v[118:121]
	v_add_f32_e32 v134, 1.0, v134
	v_rcp_f32_e32 v134, v134
	s_nop 0
	v_mul_f32_e32 v98, v134, v98
	v_and_b32_e32 v134, 0xffff0000, v140
	v_mul_f32_e32 v134, 0xbfb8aa3b, v134
	v_exp_f32_e32 v134, v134
	v_add_u32_e32 v98, 0x8000, v98
	v_add_f32_e32 v134, 1.0, v134
	v_rcp_f32_e32 v134, v134
	s_nop 0
	v_mul_f32_e32 v99, v134, v99
	v_lshlrev_b32_e32 v134, 16, v141
	v_mul_f32_e32 v134, 0xbfb8aa3b, v134
	v_exp_f32_e32 v134, v134
	v_add_u32_e32 v99, 0x8000, v99
	v_perm_b32 v98, v99, v98, s33
	v_add_f32_e32 v134, 1.0, v134
	v_rcp_f32_e32 v134, v134
	s_nop 0
	v_mul_f32_e32 v100, v134, v100
	v_and_b32_e32 v134, 0xffff0000, v141
	v_mul_f32_e32 v134, 0xbfb8aa3b, v134
	v_exp_f32_e32 v134, v134
	v_ashrrev_i32_e32 v147, 31, v146
	v_add_u32_e32 v100, 0x8000, v100
	v_lshlrev_b64 v[186:187], 1, v[146:147]
	v_add_f32_e32 v134, 1.0, v134
	v_rcp_f32_e32 v134, v134
	s_nop 0
	v_mul_f32_e32 v101, v134, v101
	v_add_u32_e32 v99, 0x8000, v101
	v_perm_b32 v99, v99, v100, s33
	v_lshl_add_u64 v[100:101], v[144:145], 0, v[186:187]
	global_store_dwordx2 v[100:101], v[98:99], off
	ds_read_b128 v[98:101], v248 offset:38912
	s_waitcnt lgkmcnt(0)
	v_mfma_f32_16x16x32_bf16 v[114:117], v[98:101], v[114:117], 0
	v_add_u32_e32 v134, 16, v188
	v_ashrrev_i32_e32 v135, 31, v134
	v_lshlrev_b64 v[134:135], 12, v[134:135]
	s_nop 4
	v_fma_f32 v0, v108, v118, v114
	s_waitcnt vmcnt(3)
	v_lshlrev_b32_e32 v114, 16, v142
	v_mul_f32_e32 v114, 0xbfb8aa3b, v114
	v_exp_f32_e32 v114, v114
	v_mul_f32_e32 v0, v110, v0
	v_fmac_f32_e32 v117, v108, v121
	v_add_f32_e32 v114, 1.0, v114
	v_rcp_f32_e32 v114, v114
	s_nop 0
	v_mul_f32_e32 v0, v114, v0
	v_fma_f32 v114, v108, v119, v115
	v_and_b32_e32 v115, 0xffff0000, v142
	v_mul_f32_e32 v115, 0xbfb8aa3b, v115
	v_exp_f32_e32 v115, v115
	v_mul_f32_e32 v114, v110, v114
	v_add_u32_e32 v0, 0x8000, v0
	v_add_f32_e32 v115, 1.0, v115
	v_rcp_f32_e32 v115, v115
	s_nop 0
	v_mul_f32_e32 v114, v115, v114
	v_fma_f32 v115, v108, v120, v116
	v_lshlrev_b32_e32 v116, 16, v143
	v_mul_f32_e32 v116, 0xbfb8aa3b, v116
	v_exp_f32_e32 v116, v116
	v_mul_f32_e32 v115, v110, v115
	v_mul_f32_e32 v108, v110, v117
	v_and_b32_e32 v110, 0xffff0000, v143
	v_add_f32_e32 v116, 1.0, v116
	s_nop 0
	s_nop 0
	v_mul_f32_e32 v110, 0xbfb8aa3b, v110
	v_exp_f32_e32 v110, v110
	s_nop 0
	s_nop 0
	s_nop 0
	s_nop 0
	s_nop 0
	s_nop 0
	s_nop 0
	s_nop 0
	v_rcp_f32_e32 v116, v116
	s_nop 0
	v_add_f32_e32 v110, 1.0, v110
	v_mul_f32_e32 v115, v116, v115
	s_nop 0
	s_nop 0
	v_ashrrev_i32_e32 v123, 31, v122
	v_lshlrev_b64 v[184:185], 1, v[122:123]
	s_mov_b32 s56, 0x62000
	s_nop 0
	s_nop 0
	s_nop 0
	s_nop 0
	s_nop 0
	s_nop 0
	s_nop 0
	s_nop 0
	v_rcp_f32_e32 v110, v110
	s_nop 0
	v_mul_f32_e32 v108, v110, v108
	v_add_u32_e32 v110, 0x8000, v114
	v_perm_b32 v114, v110, v0, s33
	v_add_u32_e32 v0, 0x8000, v108
	v_add_u32_e32 v108, 0x8000, v115
	v_perm_b32 v115, v0, v108, s33
	v_lshl_add_u64 v[116:117], v[144:145], 0, v[184:185]
	global_store_dwordx2 v[116:117], v[114:115], off
	v_add_co_u32_e32 v114, vcc, s56, v138
	v_add_u32_e32 v0, v179, v234
	s_nop 0
	v_addc_co_u32_e32 v115, vcc, 0, v139, vcc
	global_load_dwordx2 v[152:153], v[114:115], off
	global_load_dwordx2 v[148:149], v[114:115], off offset:32
	ds_read_b128 v[114:117], v181
	ds_read_b128 v[118:121], v181 offset:64
	ds_read_b128 v[122:125], v181 offset:128
	ds_read_b128 v[126:129], v181 offset:192
	s_waitcnt lgkmcnt(3)
; #define LAS __attribute__((address_space(3)))
; __device__ __forceinline__ unsigned pk2(float lo, float hi) { return __builtin_amdgcn_perm(__builtin_bit_cast(unsigned, hi) + 0x8000u, __builtin_bit_cast(unsigned, lo) + 0x8000u, 0x07060302u); }
; __device__ __forceinline__ float sigmoidf_(float x) { return 1.0f / (1.0f + __expf(-x)); }
; __device__ __forceinline__ void ph_mlstm_out(const Frame& F) {
;     ...
;         for (int tt = 0; tt < 8; ++tt) {
;             const int t = 16 * tt + l15;
;             const v2u ogc[2] = {ogn0, ogn1};
;             if (tt < 7) { ogn0 = *(const v2u*)(ogp + (size_t)(16 * (tt + 1)) * 6144); ogn1 = *(const v2u*)(ogp + (size_t)(16 * (tt + 1)) * 6144 + 16); }
;             bf16x8 qf[4];
; #pragma unroll
;             for (int st = 0; st < 4; ++st) qf[st] = *(const LAS bf16x8*)(lds + MLO_Q_OFF + t * ML_ROW + 16 * g + 64 * st);
;             const int nst = (tt >> 1) + 1;
;             bf16x8 pf[4];
; #pragma unroll
;             for (int st = 0; st < 4; ++st) if (st < nst) pf[st] = *(const LAS bf16x8*)(lds + ML_K_OFF + t * ML_ROW + 16 * g + 64 * st);
;             const float ai = ais[t], rd = rds[t];
; #pragma unroll
;             for (int vt = 0; vt < 2; ++vt) {
;                 f32x4 ci = (f32x4){0.f, 0.f, 0.f, 0.f}, cx = (f32x4){0.f, 0.f, 0.f, 0.f};
; #pragma unroll
;                 for (int st = 0; st < 4; ++st) ci = __builtin_amdgcn_mfma_f32_16x16x32_bf16(cf[vt][st], qf[st], ci, 0, 0, 0);
;                 const LAS unsigned char* vr = lds + ML_V_OFF + (16 * (2 * wave + vt) + l15) * ML_ROW + 16 * g;
; #pragma unroll
;                 for (int st = 0; st < 4; ++st) if (st < nst) cx = __builtin_amdgcn_mfma_f32_16x16x32_bf16(*(const LAS bf16x8*)(vr + 64 * st), pf[st], cx, 0, 0, 0);
;                 const int vcol = h * 256 + 16 * (2 * wave + vt) + 4 * g;
;                 const v2u ogw = ogc[vt];
;                 const float y0 = (ai * ci[0] + cx[0]) * rd * sigmoidf_(bflo(ogw.x)), y1 = (ai * ci[1] + cx[1]) * rd * sigmoidf_(bfhi(ogw.x));
;                 const float y2 = (ai * ci[2] + cx[2]) * rd * sigmoidf_(bflo(ogw.y)), y3 = (ai * ci[3] + cx[3]) * rd * sigmoidf_(bfhi(ogw.y));
;                 v2u w; w.x = pk2(y0, y1); w.y = pk2(y2, y3);
;                 *(v2u*)(YB + (size_t)(t0 + t) * 2048 + vcol) = w;
;             }
;         }
	v_mfma_f32_16x16x32_bf16 v[140:143], v[94:97], v[114:117], 0
	ds_read_b128 v[130:133], v0 offset:4096
	s_waitcnt vmcnt(5)
	v_lshlrev_b32_e32 v110, 16, v112
	v_mul_f32_e32 v110, 0xbfb8aa3b, v110
	s_waitcnt lgkmcnt(3)
	v_mfma_f32_16x16x32_bf16 v[140:143], v[82:85], v[118:121], v[140:143]
	v_exp_f32_e32 v110, v110
	v_lshl_add_u64 v[144:145], s[22:23], 0, v[134:135]
	v_and_b32_e32 v112, 0xffff0000, v112
	s_waitcnt lgkmcnt(2)
	v_mfma_f32_16x16x32_bf16 v[140:143], v[86:89], v[122:125], v[140:143]
	v_add_f32_e32 v110, 1.0, v110
	v_mul_f32_e32 v112, 0xbfb8aa3b, v112
	v_exp_f32_e32 v112, v112
	s_waitcnt lgkmcnt(0)
	v_mfma_f32_16x16x32_bf16 v[134:137], v[102:105], v[130:133], 0
	v_add_f32_e32 v112, 1.0, v112
	v_mfma_f32_16x16x32_bf16 v[140:143], v[90:93], v[126:129], v[140:143]
	v_mfma_f32_16x16x32_bf16 v[130:133], v[98:101], v[130:133], 0
	s_nop 6
	v_fma_f32 v108, v109, v140, v134
	s_nop 0
	s_nop 0
	v_mul_f32_e32 v108, v111, v108
	v_fmac_f32_e32 v137, v109, v143
	s_nop 0
	s_nop 0
	s_nop 0
	s_nop 0
	s_nop 0
	s_nop 0
	s_nop 0
	s_nop 0
	v_rcp_f32_e32 v110, v110
	s_nop 0
	v_div_scale_f32 v134, s[56:57], v112, v112, 1.0
	v_mul_f32_e32 v108, v110, v108
	v_fma_f32 v110, v109, v141, v135
	v_rcp_f32_e32 v135, v134
	v_mul_f32_e32 v110, v111, v110
	v_add_u32_e32 v108, 0x8000, v108
	v_fma_f32 v140, -v134, v135, 1.0
	v_fmac_f32_e32 v135, v140, v135
	v_div_scale_f32 v140, vcc, 1.0, v112, 1.0
	v_mul_f32_e32 v141, v140, v135
	v_fma_f32 v146, -v134, v141, v140
	v_fmac_f32_e32 v141, v146, v135
	v_fma_f32 v134, -v134, v141, v140
	v_div_fmas_f32 v134, v134, v135, v141
	v_div_fixup_f32 v112, v134, v112, 1.0
	v_lshlrev_b32_e32 v134, 16, v113
	v_mul_f32_e32 v134, 0xbfb8aa3b, v134
	v_exp_f32_e32 v134, v134
	v_mul_f32_e32 v110, v112, v110
	v_fma_f32 v112, v109, v142, v136
	v_and_b32_e32 v113, 0xffff0000, v113
	v_add_f32_e32 v134, 1.0, v134
	s_nop 0
	s_nop 0
	v_mul_f32_e32 v113, 0xbfb8aa3b, v113
	v_exp_f32_e32 v113, v113
	v_mul_f32_e32 v112, v111, v112
	s_nop 0
	s_nop 0
	s_nop 0
	s_nop 0
	s_nop 0
	s_nop 0
	s_nop 0
	s_nop 0
	v_add_f32_e32 v113, 1.0, v113
	v_rcp_f32_e32 v134, v134
	s_nop 0
	v_div_scale_f32 v135, s[56:57], v113, v113, 1.0
	v_rcp_f32_e32 v136, v135
	v_mul_f32_e32 v134, v134, v112
	v_mul_f32_e32 v112, v111, v137
	v_add_u32_e32 v110, 0x8000, v110
	v_fma_f32 v137, -v135, v136, 1.0
	v_fmac_f32_e32 v136, v137, v136
	v_div_scale_f32 v137, vcc, 1.0, v113, 1.0
	v_mul_f32_e32 v140, v137, v136
	v_fma_f32 v141, -v135, v140, v137
	v_fmac_f32_e32 v140, v141, v136
	v_fma_f32 v135, -v135, v140, v137
	v_div_fmas_f32 v135, v135, v136, v140
	v_div_fixup_f32 v113, v135, v113, 1.0
	v_mul_f32_e32 v113, v113, v112
	v_perm_b32 v112, v110, v108, s33
	v_add_u32_e32 v108, 0x8000, v113
	v_add_u32_e32 v110, 0x8000, v134
	v_perm_b32 v113, v108, v110, s33
	v_lshl_add_u64 v[134:135], v[144:145], 0, v[186:187]
	global_store_dwordx2 v[134:135], v[112:113], off
	v_mfma_f32_16x16x32_bf16 v[112:115], v[78:81], v[114:117], 0
	s_waitcnt vmcnt(5)
	v_lshlrev_b32_e32 v110, 16, v106
	v_mul_f32_e32 v110, 0xbfb8aa3b, v110
	v_exp_f32_e32 v110, v110
	v_mfma_f32_16x16x32_bf16 v[112:115], v[66:69], v[118:121], v[112:115]
	v_and_b32_e32 v106, 0xffff0000, v106
	v_mul_f32_e32 v106, 0xbfb8aa3b, v106
	v_add_f32_e32 v110, 1.0, v110
	v_mfma_f32_16x16x32_bf16 v[112:115], v[70:73], v[122:125], v[112:115]
	v_exp_f32_e32 v106, v106
	s_nop 0
	v_add_f32_e32 v106, 1.0, v106
	v_mfma_f32_16x16x32_bf16 v[112:115], v[74:77], v[126:129], v[112:115]
	s_nop 7
	v_fma_f32 v108, v109, v112, v130
	s_nop 0
	s_nop 0
	v_mul_f32_e32 v108, v111, v108
	v_fmac_f32_e32 v133, v109, v115
	s_nop 0
	s_nop 0
	s_nop 0
	s_nop 0
	s_nop 0
	s_nop 0
	s_nop 0
	s_nop 0
	v_rcp_f32_e32 v110, v110
	s_nop 0
	v_div_scale_f32 v112, s[56:57], v106, v106, 1.0
	v_mul_f32_e32 v108, v110, v108
	v_fma_f32 v110, v109, v113, v131
	v_rcp_f32_e32 v113, v112
	v_mul_f32_e32 v110, v111, v110
	v_add_u32_e32 v108, 0x8000, v108
	v_fma_f32 v116, -v112, v113, 1.0
	v_fmac_f32_e32 v113, v116, v113
	v_div_scale_f32 v116, vcc, 1.0, v106, 1.0
	v_mul_f32_e32 v117, v116, v113
	v_fma_f32 v118, -v112, v117, v116
	v_fmac_f32_e32 v117, v118, v113
	v_fma_f32 v112, -v112, v117, v116
	v_div_fmas_f32 v112, v112, v113, v117
	v_div_fixup_f32 v106, v112, v106, 1.0
	v_lshlrev_b32_e32 v112, 16, v107
	v_mul_f32_e32 v112, 0xbfb8aa3b, v112
	v_exp_f32_e32 v112, v112
	v_mul_f32_e32 v106, v106, v110
	v_fma_f32 v110, v109, v114, v132
	v_and_b32_e32 v107, 0xffff0000, v107
	v_add_f32_e32 v112, 1.0, v112
	s_nop 0
	s_nop 0
	v_mul_f32_e32 v107, 0xbfb8aa3b, v107
	v_exp_f32_e32 v107, v107
	v_mul_f32_e32 v110, v111, v110
	s_nop 0
	s_nop 0
	s_nop 0
	s_nop 0
	s_nop 0
	s_nop 0
	s_nop 0
	s_nop 0
	v_add_f32_e32 v107, 1.0, v107
	v_rcp_f32_e32 v112, v112
	s_nop 0
	v_mul_f32_e32 v109, v111, v133
	v_div_scale_f32 v111, s[56:57], v107, v107, 1.0
	v_mul_f32_e32 v110, v112, v110
	v_rcp_f32_e32 v112, v111
	v_add_u32_e32 v106, 0x8000, v106
	v_perm_b32 v106, v106, v108, s33
	v_add_u32_e32 v108, 0x8000, v110
	v_fma_f32 v113, -v111, v112, 1.0
	v_fmac_f32_e32 v112, v113, v112
	v_div_scale_f32 v113, vcc, 1.0, v107, 1.0
	v_mul_f32_e32 v114, v113, v112
	v_fma_f32 v115, -v111, v114, v113
	v_fmac_f32_e32 v114, v115, v112
	v_fma_f32 v111, -v111, v114, v113
	v_div_fmas_f32 v111, v111, v112, v114
	v_div_fixup_f32 v107, v111, v107, 1.0
	v_mul_f32_e32 v107, v107, v109
	v_add_u32_e32 v107, 0x8000, v107
	v_perm_b32 v107, v107, v108, s33
	v_lshl_add_u64 v[108:109], v[144:145], 0, v[184:185]
	s_mov_b32 s56, 0x92000
	global_store_dwordx2 v[108:109], v[106:107], off
	v_add_co_u32_e32 v106, vcc, s56, v138
	s_nop 1
	v_addc_co_u32_e32 v107, vcc, 0, v139, vcc
	global_load_dwordx2 v[146:147], v[106:107], off
	global_load_dwordx2 v[140:141], v[106:107], off offset:32
	ds_read_b128 v[114:117], v181 offset:4352
	ds_read_b128 v[118:121], v181 offset:4416
	ds_read_b128 v[122:125], v181 offset:4480
	ds_read_b128 v[126:129], v181 offset:4544
	ds_read_b128 v[110:113], v0 offset:8448
	ds_read_b128 v[130:133], v0 offset:8512
	ds_read2_b32 v[142:143], v158 offset0:160 offset1:176
	ds_read2_b32 v[144:145], v159 offset0:32 offset1:48
	v_add_u32_e32 v106, 32, v188
	s_waitcnt lgkmcnt(7)
; #define LAS __attribute__((address_space(3)))
; __device__ __forceinline__ unsigned pk2(float lo, float hi) { return __builtin_amdgcn_perm(__builtin_bit_cast(unsigned, hi) + 0x8000u, __builtin_bit_cast(unsigned, lo) + 0x8000u, 0x07060302u); }
; __device__ __forceinline__ float sigmoidf_(float x) { return 1.0f / (1.0f + __expf(-x)); }
; __device__ __forceinline__ void ph_mlstm_out(const Frame& F) {
;     ...
;         for (int tt = 0; tt < 8; ++tt) {
;             const int t = 16 * tt + l15;
;             const v2u ogc[2] = {ogn0, ogn1};
;             if (tt < 7) { ogn0 = *(const v2u*)(ogp + (size_t)(16 * (tt + 1)) * 6144); ogn1 = *(const v2u*)(ogp + (size_t)(16 * (tt + 1)) * 6144 + 16); }
;             bf16x8 qf[4];
; #pragma unroll
;             for (int st = 0; st < 4; ++st) qf[st] = *(const LAS bf16x8*)(lds + MLO_Q_OFF + t * ML_ROW + 16 * g + 64 * st);
;             const int nst = (tt >> 1) + 1;
;             bf16x8 pf[4];
; #pragma unroll
;             for (int st = 0; st < 4; ++st) if (st < nst) pf[st] = *(const LAS bf16x8*)(lds + ML_K_OFF + t * ML_ROW + 16 * g + 64 * st);
;             const float ai = ais[t], rd = rds[t];
; #pragma unroll
;             for (int vt = 0; vt < 2; ++vt) {
;                 f32x4 ci = (f32x4){0.f, 0.f, 0.f, 0.f}, cx = (f32x4){0.f, 0.f, 0.f, 0.f};
; #pragma unroll
;                 for (int st = 0; st < 4; ++st) ci = __builtin_amdgcn_mfma_f32_16x16x32_bf16(cf[vt][st], qf[st], ci, 0, 0, 0);
;                 const LAS unsigned char* vr = lds + ML_V_OFF + (16 * (2 * wave + vt) + l15) * ML_ROW + 16 * g;
; #pragma unroll
;                 for (int st = 0; st < 4; ++st) if (st < nst) cx = __builtin_amdgcn_mfma_f32_16x16x32_bf16(*(const LAS bf16x8*)(vr + 64 * st), pf[st], cx, 0, 0, 0);
;                 const int vcol = h * 256 + 16 * (2 * wave + vt) + 4 * g;
;                 const v2u ogw = ogc[vt];
;                 const float y0 = (ai * ci[0] + cx[0]) * rd * sigmoidf_(bflo(ogw.x)), y1 = (ai * ci[1] + cx[1]) * rd * sigmoidf_(bfhi(ogw.x));
;                 const float y2 = (ai * ci[2] + cx[2]) * rd * sigmoidf_(bflo(ogw.y)), y3 = (ai * ci[3] + cx[3]) * rd * sigmoidf_(bfhi(ogw.y));
;                 v2u w; w.x = pk2(y0, y1); w.y = pk2(y2, y3);
;                 *(v2u*)(YB + (size_t)(t0 + t) * 2048 + vcol) = w;
;             }
;         }
	v_mfma_f32_16x16x32_bf16 v[154:157], v[94:97], v[114:117], 0
	v_ashrrev_i32_e32 v107, 31, v106
	v_lshlrev_b64 v[106:107], 12, v[106:107]
	v_lshl_add_u64 v[150:151], s[22:23], 0, v[106:107]
	ds_read_b128 v[106:109], v247 offset:38976
	s_waitcnt lgkmcnt(7)
	v_mfma_f32_16x16x32_bf16 v[154:157], v[82:85], v[118:121], v[154:157]
	s_waitcnt lgkmcnt(4)
	v_mfma_f32_16x16x32_bf16 v[134:137], v[102:105], v[110:113], 0
	v_mfma_f32_16x16x32_bf16 v[154:157], v[86:89], v[122:125], v[154:157]
	s_waitcnt lgkmcnt(0)
	v_mfma_f32_16x16x32_bf16 v[134:137], v[106:109], v[130:133], v[134:137]
	v_mfma_f32_16x16x32_bf16 v[154:157], v[90:93], v[126:129], v[154:157]
	v_mfma_f32_16x16x32_bf16 v[114:117], v[78:81], v[114:117], 0
	v_mfma_f32_16x16x32_bf16 v[114:117], v[66:69], v[118:121], v[114:117]
	s_nop 5
	v_fma_f32 v134, v142, v154, v134
	s_waitcnt vmcnt(5)
	v_lshlrev_b32_e32 v154, 16, v152
	v_mul_f32_e32 v154, 0xbfb8aa3b, v154
	v_exp_f32_e32 v154, v154
	v_and_b32_e32 v152, 0xffff0000, v152
	v_mul_f32_e32 v152, 0xbfb8aa3b, v152
	v_exp_f32_e32 v152, v152
	v_add_f32_e32 v154, 1.0, v154
	v_div_scale_f32 v160, s[56:57], v154, v154, 1.0
	v_rcp_f32_e32 v161, v160
	v_mul_f32_e32 v134, v144, v134
	v_add_f32_e32 v152, 1.0, v152
	v_fma_f32 v135, v142, v155, v135
	v_fma_f32 v164, -v160, v161, 1.0
	v_fmac_f32_e32 v161, v164, v161
	v_div_scale_f32 v164, vcc, 1.0, v154, 1.0
	v_mul_f32_e32 v165, v164, v161
	v_fma_f32 v166, -v160, v165, v164
	v_fmac_f32_e32 v165, v166, v161
	v_fma_f32 v160, -v160, v165, v164
	v_div_fmas_f32 v160, v160, v161, v165
	v_div_fixup_f32 v154, v160, v154, 1.0
	v_mul_f32_e32 v134, v154, v134
	v_div_scale_f32 v154, s[56:57], v152, v152, 1.0
	v_rcp_f32_e32 v155, v154
	v_mul_f32_e32 v135, v144, v135
	v_fma_f32 v136, v142, v156, v136
	v_mul_f32_e32 v136, v144, v136
	v_fma_f32 v160, -v154, v155, 1.0
	v_fmac_f32_e32 v155, v160, v155
	v_div_scale_f32 v160, vcc, 1.0, v152, 1.0
	v_mul_f32_e32 v161, v160, v155
	v_fma_f32 v164, -v154, v161, v160
	v_fmac_f32_e32 v161, v164, v155
	v_fma_f32 v154, -v154, v161, v160
	v_div_fmas_f32 v154, v154, v155, v161
	v_div_fixup_f32 v152, v154, v152, 1.0
	v_mul_f32_e32 v135, v152, v135
	v_lshlrev_b32_e32 v152, 16, v153
	v_mul_f32_e32 v152, 0xbfb8aa3b, v152
	v_exp_f32_e32 v152, v152
	v_fmac_f32_e32 v137, v142, v157
	s_waitcnt vmcnt(4)
	v_lshlrev_b32_e32 v118, 16, v148
	v_mul_f32_e32 v137, v144, v137
	v_add_f32_e32 v152, 1.0, v152
	s_nop 0
	s_nop 0
	v_mul_f32_e32 v118, 0xbfb8aa3b, v118
	v_add_u32_e32 v135, 0x8000, v135
	v_add_u32_e32 v134, 0x8000, v134
	s_nop 0
	s_nop 0
	s_nop 0
	s_nop 0
	s_nop 0
	s_nop 0
	s_nop 0
	s_nop 0
	v_rcp_f32_e32 v152, v152
	s_nop 0
	v_mul_f32_e32 v136, v152, v136
	v_and_b32_e32 v152, 0xffff0000, v153
	v_mul_f32_e32 v152, 0xbfb8aa3b, v152
	v_exp_f32_e32 v152, v152
	v_exp_f32_e32 v118, v118
	v_perm_b32 v134, v135, v134, s33
	v_add_u32_e32 v136, 0x8000, v136
	v_add_f32_e32 v152, 1.0, v152
	v_div_scale_f32 v153, s[56:57], v152, v152, 1.0
	v_rcp_f32_e32 v154, v153
	v_add_f32_e32 v118, 1.0, v118
	v_div_scale_f32 v119, s[56:57], v118, v118, 1.0
	v_fma_f32 v155, -v153, v154, 1.0
	v_fmac_f32_e32 v154, v155, v154
	v_div_scale_f32 v155, vcc, 1.0, v152, 1.0
	v_mul_f32_e32 v156, v155, v154
	v_fma_f32 v157, -v153, v156, v155
	v_fmac_f32_e32 v156, v157, v154
	v_fma_f32 v153, -v153, v156, v155
	v_div_fmas_f32 v153, v153, v154, v156
	v_div_fixup_f32 v152, v153, v152, 1.0
	v_mul_f32_e32 v137, v152, v137
	v_add_u32_e32 v135, 0x8000, v137
	v_perm_b32 v135, v135, v136, s33
	v_lshl_add_u64 v[136:137], v[150:151], 0, v[186:187]
	global_store_dwordx2 v[136:137], v[134:135], off
	v_mfma_f32_16x16x32_bf16 v[134:137], v[98:101], v[110:113], 0
	ds_read_b128 v[110:113], v248 offset:38976
	v_rcp_f32_e32 v120, v119
	v_add_u32_e32 v152, 48, v188
	v_mfma_f32_16x16x32_bf16 v[114:117], v[70:73], v[122:125], v[114:117]
	v_ashrrev_i32_e32 v153, 31, v152
	v_fma_f32 v121, -v119, v120, 1.0
	v_fmac_f32_e32 v120, v121, v120
	v_div_scale_f32 v121, vcc, 1.0, v118, 1.0
	s_waitcnt lgkmcnt(0)
	v_mfma_f32_16x16x32_bf16 v[130:133], v[110:113], v[130:133], v[134:137]
	v_mul_f32_e32 v122, v121, v120
	v_fma_f32 v123, -v119, v122, v121
	v_fmac_f32_e32 v122, v123, v120
	v_mfma_f32_16x16x32_bf16 v[114:117], v[74:77], v[126:129], v[114:117]
	v_fma_f32 v119, -v119, v122, v121
	v_div_fmas_f32 v119, v119, v120, v122
	v_div_fixup_f32 v118, v119, v118, 1.0
	v_lshlrev_b64 v[152:153], 12, v[152:153]
	v_lshl_add_u64 v[156:157], s[22:23], 0, v[152:153]
	s_nop 2
	v_fma_f32 v114, v142, v114, v130
	v_mul_f32_e32 v114, v144, v114
	v_mul_f32_e32 v114, v118, v114
	v_and_b32_e32 v118, 0xffff0000, v148
	v_mul_f32_e32 v118, 0xbfb8aa3b, v118
	v_exp_f32_e32 v118, v118
	v_fma_f32 v115, v142, v115, v131
	v_mul_f32_e32 v115, v144, v115
	v_fma_f32 v116, v142, v116, v132
	v_add_f32_e32 v118, 1.0, v118
	s_nop 0
	s_nop 0
	v_mul_f32_e32 v116, v144, v116
	v_fmac_f32_e32 v133, v142, v117
	v_mul_f32_e32 v117, v144, v133
	s_nop 0
	s_nop 0
	s_nop 0
	s_nop 0
	s_nop 0
	s_nop 0
	s_nop 0
	s_nop 0
	v_rcp_f32_e32 v118, v118
	s_nop 0
	v_mul_f32_e32 v115, v118, v115
	v_lshlrev_b32_e32 v118, 16, v149
	v_mul_f32_e32 v118, 0xbfb8aa3b, v118
	v_exp_f32_e32 v118, v118
	v_add_u32_e32 v115, 0x8000, v115
	v_add_u32_e32 v114, 0x8000, v114
	v_perm_b32 v114, v115, v114, s33
	v_add_f32_e32 v118, 1.0, v118
	s_nop 0
	s_nop 0
	s_waitcnt vmcnt(2)
; #define LAS __attribute__((address_space(3)))
; __device__ __forceinline__ unsigned pk2(float lo, float hi) { return __builtin_amdgcn_perm(__builtin_bit_cast(unsigned, hi) + 0x8000u, __builtin_bit_cast(unsigned, lo) + 0x8000u, 0x07060302u); }
; __device__ __forceinline__ float sigmoidf_(float x) { return 1.0f / (1.0f + __expf(-x)); }
; __device__ __forceinline__ void ph_mlstm_out(const Frame& F) {
;     ...
;         for (int tt = 0; tt < 8; ++tt) {
;             const int t = 16 * tt + l15;
;             const v2u ogc[2] = {ogn0, ogn1};
;             if (tt < 7) { ogn0 = *(const v2u*)(ogp + (size_t)(16 * (tt + 1)) * 6144); ogn1 = *(const v2u*)(ogp + (size_t)(16 * (tt + 1)) * 6144 + 16); }
;             bf16x8 qf[4];
; #pragma unroll
;             for (int st = 0; st < 4; ++st) qf[st] = *(const LAS bf16x8*)(lds + MLO_Q_OFF + t * ML_ROW + 16 * g + 64 * st);
;             const int nst = (tt >> 1) + 1;
;             bf16x8 pf[4];
; #pragma unroll
;             for (int st = 0; st < 4; ++st) if (st < nst) pf[st] = *(const LAS bf16x8*)(lds + ML_K_OFF + t * ML_ROW + 16 * g + 64 * st);
;             const float ai = ais[t], rd = rds[t];
; #pragma unroll
;             for (int vt = 0; vt < 2; ++vt) {
;                 f32x4 ci = (f32x4){0.f, 0.f, 0.f, 0.f}, cx = (f32x4){0.f, 0.f, 0.f, 0.f};
; #pragma unroll
;                 for (int st = 0; st < 4; ++st) ci = __builtin_amdgcn_mfma_f32_16x16x32_bf16(cf[vt][st], qf[st], ci, 0, 0, 0);
;                 const LAS unsigned char* vr = lds + ML_V_OFF + (16 * (2 * wave + vt) + l15) * ML_ROW + 16 * g;
; #pragma unroll
;                 for (int st = 0; st < 4; ++st) if (st < nst) cx = __builtin_amdgcn_mfma_f32_16x16x32_bf16(*(const LAS bf16x8*)(vr + 64 * st), pf[st], cx, 0, 0, 0);
;                 const int vcol = h * 256 + 16 * (2 * wave + vt) + 4 * g;
;                 const v2u ogw = ogc[vt];
;                 const float y0 = (ai * ci[0] + cx[0]) * rd * sigmoidf_(bflo(ogw.x)), y1 = (ai * ci[1] + cx[1]) * rd * sigmoidf_(bfhi(ogw.x));
;                 const float y2 = (ai * ci[2] + cx[2]) * rd * sigmoidf_(bflo(ogw.y)), y3 = (ai * ci[3] + cx[3]) * rd * sigmoidf_(bfhi(ogw.y));
;                 v2u w; w.x = pk2(y0, y1); w.y = pk2(y2, y3);
;                 *(v2u*)(YB + (size_t)(t0 + t) * 2048 + vcol) = w;
;             }
;         }
	v_lshlrev_b32_e32 v144, 16, v146
	v_mul_f32_e32 v144, 0xbfb8aa3b, v144
	v_exp_f32_e32 v144, v144
	s_nop 0
	s_nop 0
	s_nop 0
	s_nop 0
	s_nop 0
	s_nop 0
	s_nop 0
	s_nop 0
	v_rcp_f32_e32 v118, v118
	s_nop 0
	v_mul_f32_e32 v116, v118, v116
	v_and_b32_e32 v118, 0xffff0000, v149
	v_mul_f32_e32 v118, 0xbfb8aa3b, v118
	v_exp_f32_e32 v118, v118
	v_add_u32_e32 v116, 0x8000, v116
	v_add_f32_e32 v144, 1.0, v144
	v_and_b32_e32 v146, 0xffff0000, v146
	v_add_f32_e32 v118, 1.0, v118
	s_nop 0
	s_nop 0
	s_mov_b32 s56, 0xc2000
	v_mul_f32_e32 v146, 0xbfb8aa3b, v146
	v_exp_f32_e32 v146, v146
	s_nop 0
	s_nop 0
	s_nop 0
	s_nop 0
	s_nop 0
	s_nop 0
	s_nop 0
	s_nop 0
	v_rcp_f32_e32 v118, v118
	s_nop 0
	v_mul_f32_e32 v117, v118, v117
	v_add_u32_e32 v115, 0x8000, v117
	v_perm_b32 v115, v115, v116, s33
	v_lshl_add_u64 v[116:117], v[150:151], 0, v[184:185]
	global_store_dwordx2 v[116:117], v[114:115], off
	v_add_co_u32_e32 v114, vcc, s56, v138
	v_add_f32_e32 v146, 1.0, v146
	s_nop 0
	v_addc_co_u32_e32 v115, vcc, 0, v139, vcc
	global_load_dwordx2 v[150:151], v[114:115], off
	global_load_dwordx2 v[148:149], v[114:115], off offset:32
	ds_read_b128 v[114:117], v181 offset:8704
	ds_read_b128 v[118:121], v181 offset:8768
	ds_read_b128 v[122:125], v181 offset:8832
	ds_read_b128 v[126:129], v181 offset:8896
	ds_read_b128 v[130:133], v0 offset:12800
	ds_read_b128 v[134:137], v0 offset:12864
	s_waitcnt lgkmcnt(5)
	v_mfma_f32_16x16x32_bf16 v[164:167], v[94:97], v[114:117], 0
	s_waitcnt lgkmcnt(4)
	v_mfma_f32_16x16x32_bf16 v[164:167], v[82:85], v[118:121], v[164:167]
	s_waitcnt lgkmcnt(1)
	v_mfma_f32_16x16x32_bf16 v[152:155], v[102:105], v[130:133], 0
	v_mfma_f32_16x16x32_bf16 v[164:167], v[86:89], v[122:125], v[164:167]
	s_waitcnt lgkmcnt(0)
	v_mfma_f32_16x16x32_bf16 v[152:155], v[106:109], v[134:137], v[152:155]
	v_mfma_f32_16x16x32_bf16 v[164:167], v[90:93], v[126:129], v[164:167]
	v_mfma_f32_16x16x32_bf16 v[114:117], v[78:81], v[114:117], 0
	v_mfma_f32_16x16x32_bf16 v[114:117], v[66:69], v[118:121], v[114:117]
	s_nop 5
	v_fma_f32 v142, v143, v164, v152
	s_nop 0
	s_nop 0
	v_mul_f32_e32 v142, v145, v142
	s_waitcnt vmcnt(4)
	v_lshlrev_b32_e32 v118, 16, v140
	v_mul_f32_e32 v118, 0xbfb8aa3b, v118
	s_nop 0
	s_nop 0
	s_nop 0
	s_nop 0
	s_nop 0
	s_nop 0
	s_nop 0
	s_nop 0
	v_rcp_f32_e32 v144, v144
	s_nop 0
	v_div_scale_f32 v152, s[56:57], v146, v146, 1.0
	v_mul_f32_e32 v142, v144, v142
	v_fma_f32 v144, v143, v165, v153
	v_rcp_f32_e32 v153, v152
	v_mul_f32_e32 v144, v145, v144
	v_exp_f32_e32 v118, v118
	v_fmac_f32_e32 v155, v143, v167
	v_fma_f32 v160, -v152, v153, 1.0
	v_fmac_f32_e32 v153, v160, v153
	v_div_scale_f32 v160, vcc, 1.0, v146, 1.0
	v_mul_f32_e32 v161, v160, v153
	v_fma_f32 v164, -v152, v161, v160
	v_fmac_f32_e32 v161, v164, v153
	v_fma_f32 v152, -v152, v161, v160
	v_div_fmas_f32 v152, v152, v153, v161
	v_div_fixup_f32 v146, v152, v146, 1.0
	v_lshlrev_b32_e32 v152, 16, v147
	v_mul_f32_e32 v152, 0xbfb8aa3b, v152
	v_exp_f32_e32 v152, v152
	v_mul_f32_e32 v144, v146, v144
	v_fma_f32 v146, v143, v166, v154
	v_and_b32_e32 v147, 0xffff0000, v147
	v_add_f32_e32 v152, 1.0, v152
	s_nop 0
	s_nop 0
	v_mul_f32_e32 v147, 0xbfb8aa3b, v147
	v_exp_f32_e32 v147, v147
	v_mul_f32_e32 v146, v145, v146
	s_nop 0
	s_nop 0
	s_nop 0
	s_nop 0
	s_nop 0
	s_nop 0
	s_nop 0
	s_nop 0
	v_add_f32_e32 v147, 1.0, v147
	v_rcp_f32_e32 v152, v152
	s_nop 0
	v_div_scale_f32 v153, s[56:57], v147, v147, 1.0
	v_rcp_f32_e32 v154, v153
	v_add_f32_e32 v118, 1.0, v118
	v_mul_f32_e32 v152, v152, v146
	v_mul_f32_e32 v146, v145, v155
	v_fma_f32 v155, -v153, v154, 1.0
	v_div_scale_f32 v119, s[56:57], v118, v118, 1.0
	v_fmac_f32_e32 v154, v155, v154
	v_div_scale_f32 v155, vcc, 1.0, v147, 1.0
	v_rcp_f32_e32 v120, v119
	v_mul_f32_e32 v160, v155, v154
	v_fma_f32 v161, -v153, v160, v155
	v_mfma_f32_16x16x32_bf16 v[130:133], v[98:101], v[130:133], 0
	v_fmac_f32_e32 v160, v161, v154
	v_fma_f32 v153, -v153, v160, v155
	v_fma_f32 v121, -v119, v120, 1.0
	v_mfma_f32_16x16x32_bf16 v[114:117], v[70:73], v[122:125], v[114:117]
	v_div_fmas_f32 v153, v153, v154, v160
	v_fmac_f32_e32 v120, v121, v120
	v_div_scale_f32 v121, vcc, 1.0, v118, 1.0
	v_mfma_f32_16x16x32_bf16 v[130:133], v[110:113], v[134:137], v[130:133]
	v_mul_f32_e32 v122, v121, v120
	v_fma_f32 v123, -v119, v122, v121
	v_fmac_f32_e32 v122, v123, v120
	v_mfma_f32_16x16x32_bf16 v[114:117], v[74:77], v[126:129], v[114:117]
	v_fma_f32 v119, -v119, v122, v121
	v_div_fmas_f32 v119, v119, v120, v122
	v_div_fixup_f32 v118, v119, v118, 1.0
	v_div_fixup_f32 v147, v153, v147, 1.0
	v_mul_f32_e32 v147, v147, v146
	s_nop 2
	v_fma_f32 v114, v143, v114, v130
	v_mul_f32_e32 v114, v145, v114
	v_mul_f32_e32 v114, v118, v114
	v_and_b32_e32 v118, 0xffff0000, v140
	v_mul_f32_e32 v118, 0xbfb8aa3b, v118
	v_exp_f32_e32 v118, v118
	v_fma_f32 v115, v143, v115, v131
	v_mul_f32_e32 v115, v145, v115
	v_fma_f32 v116, v143, v116, v132
	v_add_f32_e32 v118, 1.0, v118
	s_nop 0
	s_nop 0
	v_mul_f32_e32 v116, v145, v116
	v_fmac_f32_e32 v133, v143, v117
	v_mul_f32_e32 v117, v145, v133
	s_nop 0
	s_nop 0
	s_nop 0
	s_nop 0
	s_nop 0
	s_nop 0
	s_nop 0
	s_nop 0
	v_rcp_f32_e32 v118, v118
	s_nop 0
	v_mul_f32_e32 v115, v118, v115
	v_lshlrev_b32_e32 v118, 16, v141
	v_mul_f32_e32 v118, 0xbfb8aa3b, v118
	v_exp_f32_e32 v118, v118
	v_add_u32_e32 v144, 0x8000, v144
	v_add_u32_e32 v142, 0x8000, v142
	v_add_u32_e32 v115, 0x8000, v115
	v_add_f32_e32 v118, 1.0, v118
	s_nop 0
	s_nop 0
	v_add_u32_e32 v114, 0x8000, v114
	v_perm_b32 v146, v144, v142, s33
	v_add_u32_e32 v142, 0x8000, v147
	s_nop 0
	s_nop 0
	s_nop 0
	s_nop 0
	s_nop 0
	s_nop 0
	s_nop 0
	s_nop 0
	v_rcp_f32_e32 v118, v118
	s_nop 0
	v_mul_f32_e32 v116, v118, v116
; #define LAS __attribute__((address_space(3)))
; __device__ __forceinline__ unsigned pk2(float lo, float hi) { return __builtin_amdgcn_perm(__builtin_bit_cast(unsigned, hi) + 0x8000u, __builtin_bit_cast(unsigned, lo) + 0x8000u, 0x07060302u); }
; __device__ __forceinline__ float sigmoidf_(float x) { return 1.0f / (1.0f + __expf(-x)); }
; __device__ __forceinline__ void ph_mlstm_out(const Frame& F) {
;     ...
;         for (int tt = 0; tt < 8; ++tt) {
;             const int t = 16 * tt + l15;
;             const v2u ogc[2] = {ogn0, ogn1};
;             if (tt < 7) { ogn0 = *(const v2u*)(ogp + (size_t)(16 * (tt + 1)) * 6144); ogn1 = *(const v2u*)(ogp + (size_t)(16 * (tt + 1)) * 6144 + 16); }
;             bf16x8 qf[4];
; #pragma unroll
;             for (int st = 0; st < 4; ++st) qf[st] = *(const LAS bf16x8*)(lds + MLO_Q_OFF + t * ML_ROW + 16 * g + 64 * st);
;             const int nst = (tt >> 1) + 1;
;             bf16x8 pf[4];
; #pragma unroll
;             for (int st = 0; st < 4; ++st) if (st < nst) pf[st] = *(const LAS bf16x8*)(lds + ML_K_OFF + t * ML_ROW + 16 * g + 64 * st);
;             const float ai = ais[t], rd = rds[t];
; #pragma unroll
;             for (int vt = 0; vt < 2; ++vt) {
;                 f32x4 ci = (f32x4){0.f, 0.f, 0.f, 0.f}, cx = (f32x4){0.f, 0.f, 0.f, 0.f};
; #pragma unroll
;                 for (int st = 0; st < 4; ++st) ci = __builtin_amdgcn_mfma_f32_16x16x32_bf16(cf[vt][st], qf[st], ci, 0, 0, 0);
;                 const LAS unsigned char* vr = lds + ML_V_OFF + (16 * (2 * wave + vt) + l15) * ML_ROW + 16 * g;
; #pragma unroll
;                 for (int st = 0; st < 4; ++st) if (st < nst) cx = __builtin_amdgcn_mfma_f32_16x16x32_bf16(*(const LAS bf16x8*)(vr + 64 * st), pf[st], cx, 0, 0, 0);
;                 const int vcol = h * 256 + 16 * (2 * wave + vt) + 4 * g;
;                 const v2u ogw = ogc[vt];
;                 const float y0 = (ai * ci[0] + cx[0]) * rd * sigmoidf_(bflo(ogw.x)), y1 = (ai * ci[1] + cx[1]) * rd * sigmoidf_(bfhi(ogw.x));
;                 const float y2 = (ai * ci[2] + cx[2]) * rd * sigmoidf_(bflo(ogw.y)), y3 = (ai * ci[3] + cx[3]) * rd * sigmoidf_(bfhi(ogw.y));
;                 v2u w; w.x = pk2(y0, y1); w.y = pk2(y2, y3);
;                 *(v2u*)(YB + (size_t)(t0 + t) * 2048 + vcol) = w;
;             }
;         }
	v_and_b32_e32 v118, 0xffff0000, v141
	v_mul_f32_e32 v118, 0xbfb8aa3b, v118
	v_exp_f32_e32 v118, v118
	v_add_u32_e32 v144, 0x8000, v152
	v_perm_b32 v114, v115, v114, s33
	v_add_u32_e32 v116, 0x8000, v116
	v_add_f32_e32 v118, 1.0, v118
	v_div_scale_f32 v119, s[56:57], v118, v118, 1.0
	v_rcp_f32_e32 v120, v119
	v_perm_b32 v147, v142, v144, s33
	v_lshl_add_u64 v[152:153], v[156:157], 0, v[186:187]
	s_mov_b32 s56, 0xf2000
	v_fma_f32 v121, -v119, v120, 1.0
	v_fmac_f32_e32 v120, v121, v120
	v_div_scale_f32 v121, vcc, 1.0, v118, 1.0
	v_mul_f32_e32 v122, v121, v120
	v_fma_f32 v123, -v119, v122, v121
	v_fmac_f32_e32 v122, v123, v120
	v_fma_f32 v119, -v119, v122, v121
	v_div_fmas_f32 v119, v119, v120, v122
	v_div_fixup_f32 v118, v119, v118, 1.0
	v_mul_f32_e32 v117, v118, v117
	v_add_u32_e32 v115, 0x8000, v117
	v_perm_b32 v115, v115, v116, s33
	v_lshl_add_u64 v[116:117], v[156:157], 0, v[184:185]
	global_store_dwordx2 v[152:153], v[146:147], off
	global_store_dwordx2 v[116:117], v[114:115], off
	v_add_co_u32_e32 v114, vcc, s56, v138
	v_add_u32_e32 v118, 64, v188
	s_nop 0
	v_addc_co_u32_e32 v115, vcc, 0, v139, vcc
	v_ashrrev_i32_e32 v119, 31, v118
	global_load_dwordx2 v[142:143], v[114:115], off
	global_load_dwordx2 v[140:141], v[114:115], off offset:32
	ds_read_b128 v[122:125], v181 offset:13056
	ds_read_b128 v[126:129], v181 offset:13120
	ds_read_b128 v[130:133], v181 offset:13184
	ds_read_b128 v[134:137], v181 offset:13248
	ds_read_b128 v[114:117], v0 offset:17152
	ds_read_b128 v[152:155], v0 offset:17216
	ds_read_b128 v[164:167], v0 offset:17280
	ds_read2_b32 v[144:145], v158 offset0:192 offset1:208
	ds_read2_b32 v[146:147], v159 offset0:64 offset1:80
	v_lshlrev_b64 v[118:119], 12, v[118:119]
	v_lshl_add_u64 v[156:157], s[22:23], 0, v[118:119]
	s_waitcnt lgkmcnt(4)
	v_mfma_f32_16x16x32_bf16 v[118:121], v[102:105], v[114:117], 0
	s_waitcnt vmcnt(5)
	v_lshlrev_b32_e32 v161, 16, v150
	v_mul_f32_e32 v161, 0xbfb8aa3b, v161
	v_exp_f32_e32 v161, v161
	v_mfma_f32_16x16x32_bf16 v[194:197], v[94:97], v[122:125], 0
	v_and_b32_e32 v150, 0xffff0000, v150
	v_mul_f32_e32 v150, 0xbfb8aa3b, v150
	v_add_f32_e32 v161, 1.0, v161
	s_waitcnt lgkmcnt(3)
	v_mfma_f32_16x16x32_bf16 v[190:193], v[106:109], v[152:155], v[118:121]
	v_div_scale_f32 v183, s[56:57], v161, v161, 1.0
	v_rcp_f32_e32 v189, v183
	s_nop 0
	ds_read_b128 v[118:121], v247 offset:39040
	v_mfma_f32_16x16x32_bf16 v[194:197], v[82:85], v[126:129], v[194:197]
	v_exp_f32_e32 v150, v150
	s_nop 0
	v_add_f32_e32 v150, 1.0, v150
	v_mfma_f32_16x16x32_bf16 v[194:197], v[86:89], v[130:133], v[194:197]
	s_waitcnt lgkmcnt(0)
	v_mfma_f32_16x16x32_bf16 v[190:193], v[118:121], v[164:167], v[190:193]
	v_mfma_f32_16x16x32_bf16 v[194:197], v[90:93], v[134:137], v[194:197]
	v_mfma_f32_16x16x32_bf16 v[122:125], v[78:81], v[122:125], 0
	v_mfma_f32_16x16x32_bf16 v[122:125], v[66:69], v[126:129], v[122:125]
	s_nop 5
	v_fma_f32 v160, v144, v194, v190
	v_fma_f32 v190, -v183, v189, 1.0
	v_fmac_f32_e32 v189, v190, v189
	v_div_scale_f32 v190, vcc, 1.0, v161, 1.0
	v_mul_f32_e32 v194, v190, v189
	v_fma_f32 v198, -v183, v194, v190
	v_fmac_f32_e32 v194, v198, v189
	v_fma_f32 v183, -v183, v194, v190
	v_div_fmas_f32 v183, v183, v189, v194
	v_div_fixup_f32 v161, v183, v161, 1.0
	v_div_scale_f32 v183, s[56:57], v150, v150, 1.0
	v_rcp_f32_e32 v189, v183
	v_mul_f32_e32 v160, v146, v160
	v_mul_f32_e32 v160, v161, v160
	v_fma_f32 v161, v144, v195, v191
	v_fma_f32 v190, -v183, v189, 1.0
	v_fmac_f32_e32 v189, v190, v189
	v_div_scale_f32 v190, vcc, 1.0, v150, 1.0
	v_mul_f32_e32 v191, v190, v189
	v_fma_f32 v194, -v183, v191, v190
	v_fmac_f32_e32 v191, v194, v189
	v_fma_f32 v183, -v183, v191, v190
	v_div_fmas_f32 v183, v183, v189, v191
	v_div_fixup_f32 v150, v183, v150, 1.0
	v_lshlrev_b32_e32 v183, 16, v151
	v_mul_f32_e32 v183, 0xbfb8aa3b, v183
	v_exp_f32_e32 v183, v183
	v_and_b32_e32 v151, 0xffff0000, v151
	v_mul_f32_e32 v161, v146, v161
	v_mul_f32_e32 v151, 0xbfb8aa3b, v151
	v_add_f32_e32 v183, 1.0, v183
	v_div_scale_f32 v189, s[56:57], v183, v183, 1.0
	v_rcp_f32_e32 v190, v189
	v_mul_f32_e32 v150, v150, v161
	v_fma_f32 v161, v144, v196, v192
	v_exp_f32_e32 v151, v151
	v_fma_f32 v191, -v189, v190, 1.0
	v_fmac_f32_e32 v190, v191, v190
	v_div_scale_f32 v191, vcc, 1.0, v183, 1.0
	v_mul_f32_e32 v192, v191, v190
	v_fma_f32 v194, -v189, v192, v191
	v_fmac_f32_e32 v192, v194, v190
	v_fma_f32 v189, -v189, v192, v191
	v_div_fmas_f32 v189, v189, v190, v192
	v_add_f32_e32 v151, 1.0, v151
	v_div_fixup_f32 v183, v189, v183, 1.0
	v_div_scale_f32 v189, s[56:57], v151, v151, 1.0
	v_rcp_f32_e32 v190, v189
	v_mul_f32_e32 v161, v146, v161
	v_fmac_f32_e32 v193, v144, v197
	v_mul_f32_e32 v161, v183, v161
	v_fma_f32 v191, -v189, v190, 1.0
	v_fmac_f32_e32 v190, v191, v190
	v_div_scale_f32 v191, vcc, 1.0, v151, 1.0
	v_mul_f32_e32 v192, v191, v190
	v_mul_f32_e32 v183, v146, v193
	v_fma_f32 v193, -v189, v192, v191
	v_fmac_f32_e32 v192, v193, v190
	v_fma_f32 v189, -v189, v192, v191
	v_div_fmas_f32 v189, v189, v190, v192
	s_waitcnt vmcnt(4)
	v_lshlrev_b32_e32 v126, 16, v148
	v_div_fixup_f32 v151, v189, v151, 1.0
	v_mfma_f32_16x16x32_bf16 v[114:117], v[98:101], v[114:117], 0
	v_mul_f32_e32 v126, 0xbfb8aa3b, v126
	v_mul_f32_e32 v151, v151, v183
	v_add_u32_e32 v150, 0x8000, v150
	v_add_u32_e32 v160, 0x8000, v160
	v_exp_f32_e32 v126, v126
	v_perm_b32 v150, v150, v160, s33
	v_add_u32_e32 v151, 0x8000, v151
	v_add_u32_e32 v160, 0x8000, v161
	v_perm_b32 v151, v151, v160, s33
	v_lshl_add_u64 v[160:161], v[156:157], 0, v[186:187]
	global_store_dwordx2 v[160:161], v[150:151], off
	v_mfma_f32_16x16x32_bf16 v[150:153], v[110:113], v[152:155], v[114:117]
	v_add_f32_e32 v126, 1.0, v126
	v_div_scale_f32 v127, s[56:57], v126, v126, 1.0
	s_nop 0
	ds_read_b128 v[114:117], v248 offset:39040
	v_rcp_f32_e32 v128, v127
	v_mfma_f32_16x16x32_bf16 v[122:125], v[70:73], v[130:133], v[122:125]
	v_fma_f32 v129, -v127, v128, 1.0
	v_fmac_f32_e32 v128, v129, v128
	v_div_scale_f32 v129, vcc, 1.0, v126, 1.0
	s_waitcnt lgkmcnt(0)
; #define LAS __attribute__((address_space(3)))
; __device__ __forceinline__ unsigned pk2(float lo, float hi) { return __builtin_amdgcn_perm(__builtin_bit_cast(unsigned, hi) + 0x8000u, __builtin_bit_cast(unsigned, lo) + 0x8000u, 0x07060302u); }
; __device__ __forceinline__ float sigmoidf_(float x) { return 1.0f / (1.0f + __expf(-x)); }
; __device__ __forceinline__ void ph_mlstm_out(const Frame& F) {
;     ...
;         for (int tt = 0; tt < 8; ++tt) {
;             const int t = 16 * tt + l15;
;             const v2u ogc[2] = {ogn0, ogn1};
;             if (tt < 7) { ogn0 = *(const v2u*)(ogp + (size_t)(16 * (tt + 1)) * 6144); ogn1 = *(const v2u*)(ogp + (size_t)(16 * (tt + 1)) * 6144 + 16); }
;             bf16x8 qf[4];
; #pragma unroll
;             for (int st = 0; st < 4; ++st) qf[st] = *(const LAS bf16x8*)(lds + MLO_Q_OFF + t * ML_ROW + 16 * g + 64 * st);
;             const int nst = (tt >> 1) + 1;
;             bf16x8 pf[4];
; #pragma unroll
;             for (int st = 0; st < 4; ++st) if (st < nst) pf[st] = *(const LAS bf16x8*)(lds + ML_K_OFF + t * ML_ROW + 16 * g + 64 * st);
;             const float ai = ais[t], rd = rds[t];
; #pragma unroll
;             for (int vt = 0; vt < 2; ++vt) {
;                 f32x4 ci = (f32x4){0.f, 0.f, 0.f, 0.f}, cx = (f32x4){0.f, 0.f, 0.f, 0.f};
; #pragma unroll
;                 for (int st = 0; st < 4; ++st) ci = __builtin_amdgcn_mfma_f32_16x16x32_bf16(cf[vt][st], qf[st], ci, 0, 0, 0);
;                 const LAS unsigned char* vr = lds + ML_V_OFF + (16 * (2 * wave + vt) + l15) * ML_ROW + 16 * g;
; #pragma unroll
;                 for (int st = 0; st < 4; ++st) if (st < nst) cx = __builtin_amdgcn_mfma_f32_16x16x32_bf16(*(const LAS bf16x8*)(vr + 64 * st), pf[st], cx, 0, 0, 0);
;                 const int vcol = h * 256 + 16 * (2 * wave + vt) + 4 * g;
;                 const v2u ogw = ogc[vt];
;                 const float y0 = (ai * ci[0] + cx[0]) * rd * sigmoidf_(bflo(ogw.x)), y1 = (ai * ci[1] + cx[1]) * rd * sigmoidf_(bfhi(ogw.x));
;                 const float y2 = (ai * ci[2] + cx[2]) * rd * sigmoidf_(bflo(ogw.y)), y3 = (ai * ci[3] + cx[3]) * rd * sigmoidf_(bfhi(ogw.y));
;                 v2u w; w.x = pk2(y0, y1); w.y = pk2(y2, y3);
;                 *(v2u*)(YB + (size_t)(t0 + t) * 2048 + vcol) = w;
;             }
;         }
	v_mfma_f32_16x16x32_bf16 v[150:153], v[114:117], v[164:167], v[150:153]
	v_mul_f32_e32 v130, v129, v128
	v_fma_f32 v131, -v127, v130, v129
	v_fmac_f32_e32 v130, v131, v128
	v_mfma_f32_16x16x32_bf16 v[122:125], v[74:77], v[134:137], v[122:125]
	v_fma_f32 v127, -v127, v130, v129
	v_div_fmas_f32 v127, v127, v128, v130
	v_div_fixup_f32 v126, v127, v126, 1.0
	s_nop 4
	v_fma_f32 v122, v144, v122, v150
	v_mul_f32_e32 v122, v146, v122
	v_mul_f32_e32 v122, v126, v122
	v_and_b32_e32 v126, 0xffff0000, v148
	v_mul_f32_e32 v126, 0xbfb8aa3b, v126
	v_exp_f32_e32 v126, v126
	v_fma_f32 v123, v144, v123, v151
	v_mul_f32_e32 v123, v146, v123
	v_fma_f32 v124, v144, v124, v152
	v_add_f32_e32 v126, 1.0, v126
	s_nop 0
	s_nop 0
	v_mul_f32_e32 v124, v146, v124
	v_fmac_f32_e32 v153, v144, v125
	v_mul_f32_e32 v125, v146, v153
	s_nop 0
	s_nop 0
	s_nop 0
	s_nop 0
	s_nop 0
	s_nop 0
	s_nop 0
	s_nop 0
	v_rcp_f32_e32 v126, v126
	s_nop 0
	v_mul_f32_e32 v123, v126, v123
	v_lshlrev_b32_e32 v126, 16, v149
	v_mul_f32_e32 v126, 0xbfb8aa3b, v126
	v_exp_f32_e32 v126, v126
	v_add_u32_e32 v123, 0x8000, v123
	v_add_u32_e32 v122, 0x8000, v122
	v_perm_b32 v122, v123, v122, s33
	v_add_f32_e32 v126, 1.0, v126
	s_nop 0
	s_nop 0
	s_waitcnt vmcnt(2)
	v_lshlrev_b32_e32 v146, 16, v142
	v_mul_f32_e32 v146, 0xbfb8aa3b, v146
	v_exp_f32_e32 v146, v146
	s_nop 0
	s_nop 0
	s_nop 0
	s_nop 0
	s_nop 0
	s_nop 0
	s_nop 0
	s_nop 0
	v_rcp_f32_e32 v126, v126
	s_nop 0
	v_mul_f32_e32 v124, v126, v124
	v_and_b32_e32 v126, 0xffff0000, v149
	v_mul_f32_e32 v126, 0xbfb8aa3b, v126
	v_exp_f32_e32 v126, v126
	v_add_u32_e32 v124, 0x8000, v124
	v_add_f32_e32 v146, 1.0, v146
	v_and_b32_e32 v142, 0xffff0000, v142
	v_add_f32_e32 v126, 1.0, v126
	s_nop 0
	s_nop 0
	s_mov_b32 s56, 0x122000
	v_mul_f32_e32 v142, 0xbfb8aa3b, v142
	v_exp_f32_e32 v142, v142
	s_nop 0
	s_nop 0
	s_nop 0
	s_nop 0
	s_nop 0
	s_nop 0
	s_nop 0
	s_nop 0
	v_rcp_f32_e32 v126, v126
	s_nop 0
	v_mul_f32_e32 v125, v126, v125
	v_add_u32_e32 v123, 0x8000, v125
	v_perm_b32 v123, v123, v124, s33
	v_lshl_add_u64 v[124:125], v[156:157], 0, v[184:185]
	global_store_dwordx2 v[124:125], v[122:123], off
	v_add_co_u32_e32 v122, vcc, s56, v138
	v_div_scale_f32 v160, s[56:57], v146, v146, 1.0
	s_nop 0
	v_addc_co_u32_e32 v123, vcc, 0, v139, vcc
	global_load_dwordx2 v[202:203], v[122:123], off
	global_load_dwordx2 v[198:199], v[122:123], off offset:32
	ds_read_b128 v[122:125], v181 offset:17408
	ds_read_b128 v[126:129], v181 offset:17472
	ds_read_b128 v[130:133], v181 offset:17536
	ds_read_b128 v[134:137], v181 offset:17600
	ds_read_b128 v[148:151], v0 offset:21504
	ds_read_b128 v[152:155], v0 offset:21568
	ds_read_b128 v[164:167], v0 offset:21632
	s_waitcnt lgkmcnt(6)
	v_mfma_f32_16x16x32_bf16 v[194:197], v[94:97], v[122:125], 0
	v_rcp_f32_e32 v161, v160
	v_add_f32_e32 v142, 1.0, v142
	v_add_u32_e32 v156, 0x50, v188
	s_waitcnt lgkmcnt(2)
	v_mfma_f32_16x16x32_bf16 v[190:193], v[102:105], v[148:151], 0
	v_fma_f32 v183, -v160, v161, 1.0
	v_fmac_f32_e32 v161, v183, v161
	v_div_scale_f32 v183, vcc, 1.0, v146, 1.0
	v_mfma_f32_16x16x32_bf16 v[194:197], v[82:85], v[126:129], v[194:197]
	v_mul_f32_e32 v189, v183, v161
	v_ashrrev_i32_e32 v157, 31, v156
	v_lshlrev_b64 v[156:157], 12, v[156:157]
	s_waitcnt lgkmcnt(1)
	v_mfma_f32_16x16x32_bf16 v[190:193], v[106:109], v[152:155], v[190:193]
	v_lshl_add_u64 v[156:157], s[22:23], 0, v[156:157]
	v_mfma_f32_16x16x32_bf16 v[194:197], v[86:89], v[130:133], v[194:197]
	s_waitcnt lgkmcnt(0)
	v_mfma_f32_16x16x32_bf16 v[190:193], v[118:121], v[164:167], v[190:193]
	v_mfma_f32_16x16x32_bf16 v[194:197], v[90:93], v[134:137], v[194:197]
	v_mfma_f32_16x16x32_bf16 v[122:125], v[78:81], v[122:125], 0
	v_mfma_f32_16x16x32_bf16 v[122:125], v[66:69], v[126:129], v[122:125]
	s_nop 5
	v_fma_f32 v144, v145, v194, v190
	v_fma_f32 v190, -v160, v189, v183
	v_fmac_f32_e32 v189, v190, v161
	v_fma_f32 v160, -v160, v189, v183
	v_div_fmas_f32 v160, v160, v161, v189
	v_div_fixup_f32 v146, v160, v146, 1.0
	s_nop 0
	s_nop 0
	v_mul_f32_e32 v144, v147, v144
	v_mul_f32_e32 v144, v146, v144
	v_fma_f32 v146, v145, v195, v191
	s_nop 0
	s_nop 0
	s_nop 0
	s_nop 0
	s_nop 0
	s_nop 0
	s_nop 0
	s_nop 0
	v_rcp_f32_e32 v142, v142
	s_nop 0
	v_lshlrev_b32_e32 v160, 16, v143
	v_mul_f32_e32 v160, 0xbfb8aa3b, v160
	v_exp_f32_e32 v160, v160
	v_and_b32_e32 v143, 0xffff0000, v143
	v_mul_f32_e32 v143, 0xbfb8aa3b, v143
	v_exp_f32_e32 v143, v143
	v_add_f32_e32 v160, 1.0, v160
	s_nop 0
	s_nop 0
	s_waitcnt vmcnt(4)
; #define LAS __attribute__((address_space(3)))
; __device__ __forceinline__ unsigned pk2(float lo, float hi) { return __builtin_amdgcn_perm(__builtin_bit_cast(unsigned, hi) + 0x8000u, __builtin_bit_cast(unsigned, lo) + 0x8000u, 0x07060302u); }
; __device__ __forceinline__ float sigmoidf_(float x) { return 1.0f / (1.0f + __expf(-x)); }
; __device__ __forceinline__ void ph_mlstm_out(const Frame& F) {
;     ...
;         for (int tt = 0; tt < 8; ++tt) {
;             const int t = 16 * tt + l15;
;             const v2u ogc[2] = {ogn0, ogn1};
;             if (tt < 7) { ogn0 = *(const v2u*)(ogp + (size_t)(16 * (tt + 1)) * 6144); ogn1 = *(const v2u*)(ogp + (size_t)(16 * (tt + 1)) * 6144 + 16); }
;             bf16x8 qf[4];
; #pragma unroll
;             for (int st = 0; st < 4; ++st) qf[st] = *(const LAS bf16x8*)(lds + MLO_Q_OFF + t * ML_ROW + 16 * g + 64 * st);
;             const int nst = (tt >> 1) + 1;
;             bf16x8 pf[4];
; #pragma unroll
;             for (int st = 0; st < 4; ++st) if (st < nst) pf[st] = *(const LAS bf16x8*)(lds + ML_K_OFF + t * ML_ROW + 16 * g + 64 * st);
;             const float ai = ais[t], rd = rds[t];
; #pragma unroll
;             for (int vt = 0; vt < 2; ++vt) {
;                 f32x4 ci = (f32x4){0.f, 0.f, 0.f, 0.f}, cx = (f32x4){0.f, 0.f, 0.f, 0.f};
; #pragma unroll
;                 for (int st = 0; st < 4; ++st) ci = __builtin_amdgcn_mfma_f32_16x16x32_bf16(cf[vt][st], qf[st], ci, 0, 0, 0);
;                 const LAS unsigned char* vr = lds + ML_V_OFF + (16 * (2 * wave + vt) + l15) * ML_ROW + 16 * g;
; #pragma unroll
;                 for (int st = 0; st < 4; ++st) if (st < nst) cx = __builtin_amdgcn_mfma_f32_16x16x32_bf16(*(const LAS bf16x8*)(vr + 64 * st), pf[st], cx, 0, 0, 0);
;                 const int vcol = h * 256 + 16 * (2 * wave + vt) + 4 * g;
;                 const v2u ogw = ogc[vt];
;                 const float y0 = (ai * ci[0] + cx[0]) * rd * sigmoidf_(bflo(ogw.x)), y1 = (ai * ci[1] + cx[1]) * rd * sigmoidf_(bfhi(ogw.x));
;                 const float y2 = (ai * ci[2] + cx[2]) * rd * sigmoidf_(bflo(ogw.y)), y3 = (ai * ci[3] + cx[3]) * rd * sigmoidf_(bfhi(ogw.y));
;                 v2u w; w.x = pk2(y0, y1); w.y = pk2(y2, y3);
;                 *(v2u*)(YB + (size_t)(t0 + t) * 2048 + vcol) = w;
;             }
;         }
	v_lshlrev_b32_e32 v126, 16, v140
	v_add_f32_e32 v143, 1.0, v143
	v_mul_f32_e32 v126, 0xbfb8aa3b, v126
	s_nop 0
	s_nop 0
	s_nop 0
	s_nop 0
	s_nop 0
	s_nop 0
	s_nop 0
	s_nop 0
	v_rcp_f32_e32 v160, v160
	s_nop 0
	s_nop 0
	v_exp_f32_e32 v126, v126
	s_nop 0
	v_mfma_f32_16x16x32_bf16 v[148:151], v[98:101], v[148:151], 0
	v_mul_f32_e32 v146, v147, v146
	v_add_f32_e32 v126, 1.0, v126
	s_nop 0
	v_div_scale_f32 v127, s[56:57], v126, v126, 1.0
	s_nop 0
	s_nop 0
	v_rcp_f32_e32 v128, v127
	s_nop 0
	s_nop 0
	v_mfma_f32_16x16x32_bf16 v[148:151], v[110:113], v[152:155], v[148:151]
	s_nop 0
	s_nop 0
	v_fma_f32 v129, -v127, v128, 1.0
	v_mfma_f32_16x16x32_bf16 v[122:125], v[70:73], v[130:133], v[122:125]
	s_nop 0
	v_fmac_f32_e32 v128, v129, v128
	v_div_scale_f32 v129, vcc, 1.0, v126, 1.0
	v_mfma_f32_16x16x32_bf16 v[148:151], v[114:117], v[164:167], v[148:151]
	v_mul_f32_e32 v130, v129, v128
	v_fma_f32 v131, -v127, v130, v129
	v_fmac_f32_e32 v130, v131, v128
	v_mfma_f32_16x16x32_bf16 v[122:125], v[74:77], v[134:137], v[122:125]
	v_fma_f32 v127, -v127, v130, v129
	v_div_fmas_f32 v127, v127, v128, v130
	v_div_fixup_f32 v126, v127, v126, 1.0
	v_mul_f32_e32 v142, v142, v146
	v_fma_f32 v146, v145, v196, v192
	s_nop 2
	v_fma_f32 v122, v145, v122, v148
	v_mul_f32_e32 v122, v147, v122
	v_mul_f32_e32 v122, v126, v122
	v_and_b32_e32 v126, 0xffff0000, v140
	v_mul_f32_e32 v126, 0xbfb8aa3b, v126
	v_exp_f32_e32 v126, v126
	v_fma_f32 v123, v145, v123, v149
	v_mul_f32_e32 v123, v147, v123
	v_fma_f32 v124, v145, v124, v150
	v_add_f32_e32 v126, 1.0, v126
	s_nop 0
	s_nop 0
	v_mul_f32_e32 v124, v147, v124
	v_mul_f32_e32 v146, v147, v146
	v_fmac_f32_e32 v193, v145, v197
	s_nop 0
	s_nop 0
	s_nop 0
	s_nop 0
	s_nop 0
	s_nop 0
	s_nop 0
	s_nop 0
	v_rcp_f32_e32 v126, v126
	s_nop 0
	v_mul_f32_e32 v123, v126, v123
	v_lshlrev_b32_e32 v126, 16, v141
	v_mul_f32_e32 v126, 0xbfb8aa3b, v126
	v_exp_f32_e32 v126, v126
	v_fmac_f32_e32 v151, v145, v125
	v_mul_f32_e32 v146, v160, v146
	v_mul_f32_e32 v160, v147, v193
	v_add_f32_e32 v126, 1.0, v126
	s_nop 0
	s_nop 0
	v_rcp_f32_e32 v143, v143
	s_nop 0
	v_mul_f32_e32 v125, v147, v151
	v_mul_f32_e32 v143, v143, v160
	s_nop 0
	s_nop 0
	s_nop 0
	s_nop 0
	s_nop 0
	s_nop 0
	s_nop 0
	s_nop 0
	v_rcp_f32_e32 v126, v126
	s_nop 0
	v_mul_f32_e32 v124, v126, v124
	v_and_b32_e32 v126, 0xffff0000, v141
	v_mul_f32_e32 v126, 0xbfb8aa3b, v126
	v_exp_f32_e32 v126, v126
	v_add_u32_e32 v142, 0x8000, v142
	v_add_u32_e32 v144, 0x8000, v144
	v_add_u32_e32 v123, 0x8000, v123
	v_add_f32_e32 v126, 1.0, v126
	s_nop 0
	s_nop 0
	v_add_u32_e32 v122, 0x8000, v122
	v_perm_b32 v142, v142, v144, s33
	v_add_u32_e32 v143, 0x8000, v143
	s_nop 0
	s_nop 0
	s_nop 0
	s_nop 0
	s_nop 0
	s_nop 0
	s_nop 0
	s_nop 0
	v_rcp_f32_e32 v126, v126
	s_nop 0
	v_mul_f32_e32 v125, v126, v125
	v_add_u32_e32 v144, 0x8000, v146
	v_perm_b32 v122, v123, v122, s33
	v_add_u32_e32 v123, 0x8000, v125
	v_add_u32_e32 v124, 0x8000, v124
	v_perm_b32 v143, v143, v144, s33
	v_lshl_add_u64 v[160:161], v[156:157], 0, v[186:187]
	v_perm_b32 v123, v123, v124, s33
	v_lshl_add_u64 v[124:125], v[156:157], 0, v[184:185]
	s_mov_b32 s56, 0x152000
	global_store_dwordx2 v[160:161], v[142:143], off
	global_store_dwordx2 v[124:125], v[122:123], off
	v_add_co_u32_e32 v122, vcc, s56, v138
	s_nop 1
	v_addc_co_u32_e32 v123, vcc, 0, v139, vcc
	global_load_dwordx2 v[196:197], v[122:123], off
	global_load_dwordx2 v[190:191], v[122:123], off offset:32
	v_add_u32_e32 v122, 0x60, v188
	v_ashrrev_i32_e32 v123, 31, v122
	v_lshlrev_b64 v[122:123], 12, v[122:123]
	ds_read_b128 v[130:133], v181 offset:21760
	ds_read_b128 v[134:137], v181 offset:21824
	ds_read_b128 v[138:141], v181 offset:21888
	ds_read_b128 v[142:145], v181 offset:21952
	ds_read_b128 v[126:129], v0 offset:25856
	ds_read_b128 v[150:153], v0 offset:25920
	ds_read_b128 v[154:157], v0 offset:25984
	ds_read_b128 v[146:149], v0 offset:26048
	ds_read2_b32 v[192:193], v158 offset0:224 offset1:240
	ds_read2_b32 v[194:195], v159 offset0:96 offset1:112
	v_lshl_add_u64 v[200:201], s[22:23], 0, v[122:123]
	s_waitcnt lgkmcnt(5)
	v_mfma_f32_16x16x32_bf16 v[122:125], v[102:105], v[126:129], 0
	s_waitcnt lgkmcnt(4)
	v_mfma_f32_16x16x32_bf16 v[122:125], v[106:109], v[150:153], v[122:125]
	v_mfma_f32_16x16x32_bf16 v[164:167], v[94:97], v[130:133], 0
	s_waitcnt lgkmcnt(3)
	v_mfma_f32_16x16x32_bf16 v[158:161], v[118:121], v[154:157], v[122:125]
	s_nop 4
	ds_read_b128 v[122:125], v247 offset:39104
	v_mfma_f32_16x16x32_bf16 v[164:167], v[82:85], v[134:137], v[164:167]
	v_mfma_f32_16x16x32_bf16 v[126:129], v[98:101], v[126:129], 0
	v_mfma_f32_16x16x32_bf16 v[164:167], v[86:89], v[138:141], v[164:167]
	v_mfma_f32_16x16x32_bf16 v[126:129], v[110:113], v[150:153], v[126:129]
	v_mfma_f32_16x16x32_bf16 v[164:167], v[90:93], v[142:145], v[164:167]
	v_mfma_f32_16x16x32_bf16 v[150:153], v[114:117], v[154:157], v[126:129]
	s_nop 5
	ds_read_b128 v[126:129], v248 offset:39104
	s_waitcnt lgkmcnt(1)
	v_mfma_f32_16x16x32_bf16 v[158:161], v[122:125], v[146:149], v[158:161]
	v_mfma_f32_16x16x32_bf16 v[130:133], v[78:81], v[130:133], 0
	v_mfma_f32_16x16x32_bf16 v[130:133], v[66:69], v[134:137], v[130:133]
	s_nop 5
	v_fma_f32 v158, v192, v164, v158
	s_waitcnt vmcnt(5)
	v_lshlrev_b32_e32 v164, 16, v202
	v_mul_f32_e32 v164, 0xbfb8aa3b, v164
	v_exp_f32_e32 v164, v164
	v_mul_f32_e32 v158, v194, v158
	v_fma_f32 v159, v192, v165, v159
	v_mul_f32_e32 v159, v194, v159
	v_add_f32_e32 v164, 1.0, v164
	v_div_scale_f32 v183, s[56:57], v164, v164, 1.0
	v_rcp_f32_e32 v189, v183
	v_fma_f32 v160, v192, v166, v160
	v_mul_f32_e32 v160, v194, v160
	s_waitcnt vmcnt(4)
; #define LAS __attribute__((address_space(3)))
; __device__ __forceinline__ unsigned pk2(float lo, float hi) { return __builtin_amdgcn_perm(__builtin_bit_cast(unsigned, hi) + 0x8000u, __builtin_bit_cast(unsigned, lo) + 0x8000u, 0x07060302u); }
; __device__ __forceinline__ float sigmoidf_(float x) { return 1.0f / (1.0f + __expf(-x)); }
; __device__ __forceinline__ void ph_mlstm_out(const Frame& F) {
;     ...
;         for (int tt = 0; tt < 8; ++tt) {
;             const int t = 16 * tt + l15;
;             const v2u ogc[2] = {ogn0, ogn1};
;             if (tt < 7) { ogn0 = *(const v2u*)(ogp + (size_t)(16 * (tt + 1)) * 6144); ogn1 = *(const v2u*)(ogp + (size_t)(16 * (tt + 1)) * 6144 + 16); }
;             bf16x8 qf[4];
; #pragma unroll
;             for (int st = 0; st < 4; ++st) qf[st] = *(const LAS bf16x8*)(lds + MLO_Q_OFF + t * ML_ROW + 16 * g + 64 * st);
;             const int nst = (tt >> 1) + 1;
;             bf16x8 pf[4];
; #pragma unroll
;             for (int st = 0; st < 4; ++st) if (st < nst) pf[st] = *(const LAS bf16x8*)(lds + ML_K_OFF + t * ML_ROW + 16 * g + 64 * st);
;             const float ai = ais[t], rd = rds[t];
; #pragma unroll
;             for (int vt = 0; vt < 2; ++vt) {
;                 f32x4 ci = (f32x4){0.f, 0.f, 0.f, 0.f}, cx = (f32x4){0.f, 0.f, 0.f, 0.f};
; #pragma unroll
;                 for (int st = 0; st < 4; ++st) ci = __builtin_amdgcn_mfma_f32_16x16x32_bf16(cf[vt][st], qf[st], ci, 0, 0, 0);
;                 const LAS unsigned char* vr = lds + ML_V_OFF + (16 * (2 * wave + vt) + l15) * ML_ROW + 16 * g;
; #pragma unroll
;                 for (int st = 0; st < 4; ++st) if (st < nst) cx = __builtin_amdgcn_mfma_f32_16x16x32_bf16(*(const LAS bf16x8*)(vr + 64 * st), pf[st], cx, 0, 0, 0);
;                 const int vcol = h * 256 + 16 * (2 * wave + vt) + 4 * g;
;                 const v2u ogw = ogc[vt];
;                 const float y0 = (ai * ci[0] + cx[0]) * rd * sigmoidf_(bflo(ogw.x)), y1 = (ai * ci[1] + cx[1]) * rd * sigmoidf_(bfhi(ogw.x));
;                 const float y2 = (ai * ci[2] + cx[2]) * rd * sigmoidf_(bflo(ogw.y)), y3 = (ai * ci[3] + cx[3]) * rd * sigmoidf_(bfhi(ogw.y));
;                 v2u w; w.x = pk2(y0, y1); w.y = pk2(y2, y3);
;                 *(v2u*)(YB + (size_t)(t0 + t) * 2048 + vcol) = w;
;             }
;         }
	v_lshlrev_b32_e32 v134, 16, v198
	v_fma_f32 v249, -v183, v189, 1.0
	v_fmac_f32_e32 v189, v249, v189
	v_div_scale_f32 v249, vcc, 1.0, v164, 1.0
	v_mul_f32_e32 v250, v249, v189
	v_fma_f32 v251, -v183, v250, v249
	v_fmac_f32_e32 v250, v251, v189
	v_fma_f32 v183, -v183, v250, v249
	v_div_fmas_f32 v183, v183, v189, v250
	v_div_fixup_f32 v164, v183, v164, 1.0
	v_mul_f32_e32 v158, v164, v158
	v_and_b32_e32 v164, 0xffff0000, v202
	v_mul_f32_e32 v164, 0xbfb8aa3b, v164
	v_exp_f32_e32 v164, v164
	v_mul_f32_e32 v134, 0xbfb8aa3b, v134
	v_exp_f32_e32 v134, v134
	v_fmac_f32_e32 v161, v192, v167
	v_add_f32_e32 v164, 1.0, v164
	v_div_scale_f32 v165, s[56:57], v164, v164, 1.0
	v_rcp_f32_e32 v183, v165
	v_add_f32_e32 v134, 1.0, v134
	v_div_scale_f32 v135, s[56:57], v134, v134, 1.0
	v_fma_f32 v189, -v165, v183, 1.0
	v_fmac_f32_e32 v183, v189, v183
	v_div_scale_f32 v189, vcc, 1.0, v164, 1.0
	v_mul_f32_e32 v202, v189, v183
	v_fma_f32 v249, -v165, v202, v189
	v_fmac_f32_e32 v202, v249, v183
	v_fma_f32 v165, -v165, v202, v189
	v_div_fmas_f32 v165, v165, v183, v202
	v_div_fixup_f32 v164, v165, v164, 1.0
	v_mul_f32_e32 v159, v164, v159
	v_lshlrev_b32_e32 v164, 16, v203
	v_mul_f32_e32 v164, 0xbfb8aa3b, v164
	v_exp_f32_e32 v164, v164
	v_rcp_f32_e32 v136, v135
	v_mfma_f32_16x16x32_bf16 v[130:133], v[70:73], v[138:141], v[130:133]
	v_mul_f32_e32 v161, v194, v161
	v_add_f32_e32 v164, 1.0, v164
	v_div_scale_f32 v165, s[56:57], v164, v164, 1.0
	v_rcp_f32_e32 v166, v165
	v_fma_f32 v137, -v135, v136, 1.0
	v_fmac_f32_e32 v136, v137, v136
	s_waitcnt lgkmcnt(0)
	v_mfma_f32_16x16x32_bf16 v[146:149], v[126:129], v[146:149], v[150:153]
	v_fma_f32 v183, -v165, v166, 1.0
	v_fmac_f32_e32 v166, v183, v166
	v_div_scale_f32 v183, vcc, 1.0, v164, 1.0
	v_mul_f32_e32 v189, v183, v166
	v_fma_f32 v202, -v165, v189, v183
	v_fmac_f32_e32 v189, v202, v166
	v_fma_f32 v165, -v165, v189, v183
	v_div_fmas_f32 v165, v165, v166, v189
	v_div_fixup_f32 v164, v165, v164, 1.0
	v_mul_f32_e32 v160, v164, v160
	v_and_b32_e32 v164, 0xffff0000, v203
	v_mul_f32_e32 v164, 0xbfb8aa3b, v164
	v_exp_f32_e32 v164, v164
	v_mfma_f32_16x16x32_bf16 v[130:133], v[74:77], v[142:145], v[130:133]
	v_add_u32_e32 v159, 0x8000, v159
	v_add_u32_e32 v158, 0x8000, v158
	v_add_f32_e32 v164, 1.0, v164
	v_div_scale_f32 v165, s[56:57], v164, v164, 1.0
	v_rcp_f32_e32 v166, v165
	s_nop 2
	v_fma_f32 v130, v192, v130, v146
	v_mul_f32_e32 v130, v194, v130
	v_fma_f32 v131, v192, v131, v147
	v_fma_f32 v167, -v165, v166, 1.0
	v_fmac_f32_e32 v166, v167, v166
	v_div_scale_f32 v167, vcc, 1.0, v164, 1.0
	v_mul_f32_e32 v183, v167, v166
	v_fma_f32 v189, -v165, v183, v167
	v_fmac_f32_e32 v183, v189, v166
	v_fma_f32 v165, -v165, v183, v167
	v_div_fmas_f32 v165, v165, v166, v183
	v_div_scale_f32 v137, vcc, 1.0, v134, 1.0
	v_mul_f32_e32 v138, v137, v136
	v_fma_f32 v139, -v135, v138, v137
	v_fmac_f32_e32 v138, v139, v136
	v_fma_f32 v135, -v135, v138, v137
	v_div_fmas_f32 v135, v135, v136, v138
	v_div_fixup_f32 v134, v135, v134, 1.0
	v_mul_f32_e32 v130, v134, v130
	v_and_b32_e32 v134, 0xffff0000, v198
	v_mul_f32_e32 v134, 0xbfb8aa3b, v134
	v_exp_f32_e32 v134, v134
	v_mul_f32_e32 v131, v194, v131
	v_fma_f32 v132, v192, v132, v148
	v_mul_f32_e32 v132, v194, v132
	v_add_f32_e32 v134, 1.0, v134
	s_nop 0
	s_nop 0
	v_fmac_f32_e32 v149, v192, v133
	v_div_fixup_f32 v164, v165, v164, 1.0
	v_mul_f32_e32 v133, v194, v149
	s_nop 0
	s_nop 0
	s_nop 0
	s_nop 0
	s_nop 0
	s_nop 0
	s_nop 0
	s_nop 0
	v_rcp_f32_e32 v134, v134
	s_nop 0
	v_mul_f32_e32 v131, v134, v131
	v_lshlrev_b32_e32 v134, 16, v199
	v_mul_f32_e32 v134, 0xbfb8aa3b, v134
	v_exp_f32_e32 v134, v134
	v_mul_f32_e32 v161, v164, v161
	v_add_u32_e32 v131, 0x8000, v131
	v_add_u32_e32 v130, 0x8000, v130
	v_add_f32_e32 v134, 1.0, v134
	s_nop 0
	s_nop 0
	v_perm_b32 v158, v159, v158, s33
	v_add_u32_e32 v159, 0x8000, v161
	v_add_u32_e32 v160, 0x8000, v160
	s_nop 0
	s_nop 0
	s_nop 0
	s_nop 0
	s_nop 0
	s_nop 0
	s_nop 0
	s_nop 0
	v_rcp_f32_e32 v134, v134
	s_nop 0
	v_mul_f32_e32 v132, v134, v132
	v_and_b32_e32 v134, 0xffff0000, v199
	v_mul_f32_e32 v134, 0xbfb8aa3b, v134
	v_exp_f32_e32 v134, v134
	v_perm_b32 v130, v131, v130, s33
	v_add_u32_e32 v132, 0x8000, v132
	v_perm_b32 v159, v159, v160, s33
	v_add_f32_e32 v134, 1.0, v134
	s_nop 0
	s_nop 0
	v_lshl_add_u64 v[160:161], v[200:201], 0, v[186:187]
	global_store_dwordx2 v[160:161], v[158:159], off
	v_add_u32_e32 v164, 0x70, v188
	s_nop 0
	s_nop 0
	s_nop 0
	s_nop 0
	s_nop 0
	s_nop 0
	s_nop 0
	s_nop 0
	v_rcp_f32_e32 v134, v134
	s_nop 0
	v_mul_f32_e32 v133, v134, v133
	v_add_u32_e32 v131, 0x8000, v133
	v_perm_b32 v131, v131, v132, s33
	v_lshl_add_u64 v[132:133], v[200:201], 0, v[184:185]
	global_store_dwordx2 v[132:133], v[130:131], off
	ds_read_b128 v[142:145], v181 offset:26112
	ds_read_b128 v[130:133], v181 offset:26176
	ds_read_b128 v[134:137], v181 offset:26240
	ds_read_b128 v[138:141], v181 offset:26304
	ds_read_b128 v[146:149], v0 offset:30208
	ds_read_b128 v[158:161], v0 offset:30272
	ds_read_b128 v[154:157], v0 offset:30336
	ds_read_b128 v[150:153], v0 offset:30400
	s_waitcnt lgkmcnt(3)
; #define LAS __attribute__((address_space(3)))
; __device__ __forceinline__ unsigned pk2(float lo, float hi) { return __builtin_amdgcn_perm(__builtin_bit_cast(unsigned, hi) + 0x8000u, __builtin_bit_cast(unsigned, lo) + 0x8000u, 0x07060302u); }
; __device__ __forceinline__ float sigmoidf_(float x) { return 1.0f / (1.0f + __expf(-x)); }
; __device__ __forceinline__ void ph_mlstm_out(const Frame& F) {
;     ...
;         for (int tt = 0; tt < 8; ++tt) {
;             const int t = 16 * tt + l15;
;             const v2u ogc[2] = {ogn0, ogn1};
;             if (tt < 7) { ogn0 = *(const v2u*)(ogp + (size_t)(16 * (tt + 1)) * 6144); ogn1 = *(const v2u*)(ogp + (size_t)(16 * (tt + 1)) * 6144 + 16); }
;             bf16x8 qf[4];
; #pragma unroll
;             for (int st = 0; st < 4; ++st) qf[st] = *(const LAS bf16x8*)(lds + MLO_Q_OFF + t * ML_ROW + 16 * g + 64 * st);
;             const int nst = (tt >> 1) + 1;
;             bf16x8 pf[4];
; #pragma unroll
;             for (int st = 0; st < 4; ++st) if (st < nst) pf[st] = *(const LAS bf16x8*)(lds + ML_K_OFF + t * ML_ROW + 16 * g + 64 * st);
;             const float ai = ais[t], rd = rds[t];
; #pragma unroll
;             for (int vt = 0; vt < 2; ++vt) {
;                 f32x4 ci = (f32x4){0.f, 0.f, 0.f, 0.f}, cx = (f32x4){0.f, 0.f, 0.f, 0.f};
; #pragma unroll
;                 for (int st = 0; st < 4; ++st) ci = __builtin_amdgcn_mfma_f32_16x16x32_bf16(cf[vt][st], qf[st], ci, 0, 0, 0);
;                 const LAS unsigned char* vr = lds + ML_V_OFF + (16 * (2 * wave + vt) + l15) * ML_ROW + 16 * g;
; #pragma unroll
;                 for (int st = 0; st < 4; ++st) if (st < nst) cx = __builtin_amdgcn_mfma_f32_16x16x32_bf16(*(const LAS bf16x8*)(vr + 64 * st), pf[st], cx, 0, 0, 0);
;                 const int vcol = h * 256 + 16 * (2 * wave + vt) + 4 * g;
;                 const v2u ogw = ogc[vt];
;                 const float y0 = (ai * ci[0] + cx[0]) * rd * sigmoidf_(bflo(ogw.x)), y1 = (ai * ci[1] + cx[1]) * rd * sigmoidf_(bfhi(ogw.x));
;                 const float y2 = (ai * ci[2] + cx[2]) * rd * sigmoidf_(bflo(ogw.y)), y3 = (ai * ci[3] + cx[3]) * rd * sigmoidf_(bfhi(ogw.y));
;                 v2u w; w.x = pk2(y0, y1); w.y = pk2(y2, y3);
;                 *(v2u*)(YB + (size_t)(t0 + t) * 2048 + vcol) = w;
;             }
;         }
	v_mfma_f32_16x16x32_bf16 v[102:105], v[102:105], v[146:149], 0
	v_ashrrev_i32_e32 v165, 31, v164
	v_lshlrev_b64 v[164:165], 12, v[164:165]
	v_lshl_add_u64 v[188:189], s[22:23], 0, v[164:165]
	v_mfma_f32_16x16x32_bf16 v[94:97], v[94:97], v[142:145], 0
	s_waitcnt lgkmcnt(2)
	v_mfma_f32_16x16x32_bf16 v[102:105], v[106:109], v[158:161], v[102:105]
	v_mfma_f32_16x16x32_bf16 v[82:85], v[82:85], v[130:133], v[94:97]
	s_waitcnt lgkmcnt(1)
	v_mfma_f32_16x16x32_bf16 v[102:105], v[118:121], v[154:157], v[102:105]
	v_mfma_f32_16x16x32_bf16 v[82:85], v[86:89], v[134:137], v[82:85]
	s_waitcnt lgkmcnt(0)
	v_mfma_f32_16x16x32_bf16 v[102:105], v[122:125], v[150:153], v[102:105]
	v_mfma_f32_16x16x32_bf16 v[82:85], v[90:93], v[138:141], v[82:85]
	v_mfma_f32_16x16x32_bf16 v[78:81], v[78:81], v[142:145], 0
	v_mfma_f32_16x16x32_bf16 v[66:69], v[66:69], v[130:133], v[78:81]
	s_nop 5
	v_fma_f32 v0, v193, v82, v102
	s_waitcnt vmcnt(3)
	v_lshlrev_b32_e32 v82, 16, v196
	v_mul_f32_e32 v82, 0xbfb8aa3b, v82
	v_exp_f32_e32 v82, v82
	v_mul_f32_e32 v0, v195, v0
	v_fmac_f32_e32 v105, v193, v85
	v_and_b32_e32 v85, 0xffff0000, v197
	v_add_f32_e32 v82, 1.0, v82
	s_nop 0
	s_nop 0
	v_mul_f32_e32 v85, 0xbfb8aa3b, v85
	v_exp_f32_e32 v85, v85
	v_mfma_f32_16x16x32_bf16 v[66:69], v[70:73], v[134:137], v[66:69]
	s_nop 0
	s_nop 0
	s_nop 0
	s_nop 0
	s_nop 0
	s_nop 0
	s_nop 0
	s_nop 0
	v_rcp_f32_e32 v82, v82
	s_nop 0
	v_mul_f32_e32 v0, v82, v0
	v_fma_f32 v82, v193, v83, v103
	v_and_b32_e32 v83, 0xffff0000, v196
	v_mul_f32_e32 v83, 0xbfb8aa3b, v83
	v_exp_f32_e32 v83, v83
	v_mul_f32_e32 v82, v195, v82
	v_add_f32_e32 v85, 1.0, v85
	v_add_u32_e32 v0, 0x8000, v0
	v_add_f32_e32 v83, 1.0, v83
	v_mfma_f32_16x16x32_bf16 v[66:69], v[74:77], v[138:141], v[66:69]
	v_rcp_f32_e32 v83, v83
	s_nop 0
	v_mul_f32_e32 v82, v83, v82
	v_fma_f32 v83, v193, v84, v104
	v_lshlrev_b32_e32 v84, 16, v197
	v_mul_f32_e32 v84, 0xbfb8aa3b, v84
	v_exp_f32_e32 v84, v84
	v_mul_f32_e32 v83, v195, v83
	v_add_u32_e32 v82, 0x8000, v82
	v_perm_b32 v82, v82, v0, s33
	v_add_f32_e32 v84, 1.0, v84
	v_rcp_f32_e32 v84, v84
	s_nop 0
	s_nop 0
	s_nop 0
	v_mul_f32_e32 v83, v84, v83
	v_mul_f32_e32 v84, v195, v105
	v_add_u32_e32 v83, 0x8000, v83
	s_nop 0
	s_nop 0
	s_nop 0
	s_nop 0
	s_nop 0
	s_nop 0
	s_nop 0
	s_nop 0
	v_rcp_f32_e32 v85, v85
	s_nop 0
	v_mul_f32_e32 v84, v85, v84
	v_add_u32_e32 v0, 0x8000, v84
	v_perm_b32 v83, v0, v83, s33
	v_lshl_add_u64 v[84:85], v[188:189], 0, v[186:187]
	global_store_dwordx2 v[84:85], v[82:83], off
	v_mfma_f32_16x16x32_bf16 v[82:85], v[98:101], v[146:149], 0
	v_mfma_f32_16x16x32_bf16 v[82:85], v[110:113], v[158:161], v[82:85]
	v_mfma_f32_16x16x32_bf16 v[82:85], v[114:117], v[154:157], v[82:85]
	v_mfma_f32_16x16x32_bf16 v[82:85], v[126:129], v[150:153], v[82:85]
	s_nop 7
	v_fma_f32 v0, v193, v66, v82
	s_waitcnt vmcnt(3)
	v_lshlrev_b32_e32 v66, 16, v190
	v_mul_f32_e32 v66, 0xbfb8aa3b, v66
	v_exp_f32_e32 v66, v66
	v_mul_f32_e32 v0, v195, v0
	v_fmac_f32_e32 v85, v193, v69
	v_and_b32_e32 v69, 0xffff0000, v191
	v_add_f32_e32 v66, 1.0, v66
	s_nop 0
	s_nop 0
	v_mul_f32_e32 v69, 0xbfb8aa3b, v69
	v_exp_f32_e32 v69, v69
	s_nop 0
	s_nop 0
	s_nop 0
	s_nop 0
	s_nop 0
	s_nop 0
	s_nop 0
	s_nop 0
	v_rcp_f32_e32 v66, v66
	s_nop 0
	v_mul_f32_e32 v0, v66, v0
	v_fma_f32 v66, v193, v67, v83
	v_and_b32_e32 v67, 0xffff0000, v190
	v_mul_f32_e32 v67, 0xbfb8aa3b, v67
	v_exp_f32_e32 v67, v67
	v_mul_f32_e32 v66, v195, v66
	v_add_f32_e32 v69, 1.0, v69
	v_add_u32_e32 v0, 0x8000, v0
	v_add_f32_e32 v67, 1.0, v67
	v_rcp_f32_e32 v67, v67
	s_nop 0
	v_mul_f32_e32 v66, v67, v66
	v_fma_f32 v67, v193, v68, v84
	v_lshlrev_b32_e32 v68, 16, v191
	v_mul_f32_e32 v68, 0xbfb8aa3b, v68
	v_exp_f32_e32 v68, v68
	v_mul_f32_e32 v67, v195, v67
	v_add_u32_e32 v66, 0x8000, v66
	v_perm_b32 v66, v66, v0, s33
	v_add_f32_e32 v68, 1.0, v68
	v_rcp_f32_e32 v68, v68
	s_nop 0
	s_nop 0
	s_nop 0
	v_mul_f32_e32 v67, v68, v67
	v_mul_f32_e32 v68, v195, v85
	v_add_u32_e32 v67, 0x8000, v67
	s_nop 0
	s_nop 0
	s_nop 0
	s_nop 0
	s_nop 0
	s_nop 0
	s_nop 0
	s_nop 0
	v_rcp_f32_e32 v69, v69
	s_nop 0
	v_mul_f32_e32 v68, v69, v68
	v_add_u32_e32 v0, 0x8000, v68
	v_perm_b32 v67, v0, v67, s33
	v_lshl_add_u64 v[68:69], v[188:189], 0, v[184:185]
	s_andn2_b64 vcc, exec, s[54:55]
	s_mov_b32 s56, s21
	global_store_dwordx2 v[68:69], v[66:67], off
	s_cbranch_vccz .LBB0_623
